# speedup vs baseline: 1.0063x; 1.0063x over previous
.Lc_go:
	s_cmp_eq_u32 s45, 0
	s_cbranch_scc0 .Lc_par1
	ds_read2_b64 v[48:51], v32 offset0:0 offset1:202
	ds_read_b128 v[120:123], v33 offset:0
	ds_read2_b64 v[10:13], v34 offset0:0 offset1:202
	ds_read2_b64 v[52:55], v32 offset0:1 offset1:203
	ds_read2_b64 v[56:59], v32 offset0:2 offset1:204
	ds_read_b128 v[124:127], v33 offset:16
	ds_read2_b64 v[60:63], v32 offset0:3 offset1:205
	s_mov_b32 s70, 0
	s_mov_b32 s71, 0
.Lc0_loop:
	s_waitcnt lgkmcnt(3)
	v_pk_fma_f16 v6, v2, v120, v121 op_sel:[0,0,0] op_sel_hi:[1,0,0] neg_lo:[1,0,0] neg_hi:[1,0,0]
	v_pk_fma_f16 v7, v3, v120, v121 op_sel:[0,0,0] op_sel_hi:[1,0,0] neg_lo:[1,0,0] neg_hi:[1,0,0]
	v_pk_fma_f16 v8, v4, v120, v121 op_sel:[0,0,0] op_sel_hi:[1,0,0] neg_lo:[1,0,0] neg_hi:[1,0,0]
	v_pk_fma_f16 v9, v5, v120, v121 op_sel:[0,0,0] op_sel_hi:[1,0,0] neg_lo:[1,0,0] neg_hi:[1,0,0]
	v_mfma_f32_16x16x32_f16 v[18:21], v[10:13], v[2:5], 0
	ds_read2_b64 v[64:67], v32 offset0:4 offset1:206
	ds_read_b128 v[128:131], v33 offset:32
	ds_read_b32 v37, v36 offset:4
	ds_read_b32 v38, v36 offset:68
	v_pk_fma_f16 v2, v48, v6, v2
	v_pk_fma_f16 v3, v49, v7, v3
	v_pk_fma_f16 v4, v50, v8, v4
	v_pk_fma_f16 v5, v51, v9, v5
	v_cndmask_b32_e64 v29, v29, v25, s[66:67]
	v_cvt_pk_f16_f32 v30, v26, v27
	v_cvt_pk_f16_f32 v31, v28, v29
	ds_write_b16 v39, v30 offset:0
	ds_write_b16_d16_hi v39, v30 offset:64
	ds_write_b16 v39, v31 offset:128
	ds_write_b16_d16_hi v39, v31 offset:192
	s_mov_b64 exec, 1
	ds_add_u32 v36, v44 offset:124
	s_mov_b64 exec, -1
	v_pk_fma_f16 v6, v2, v122, v123 op_sel:[0,0,0] op_sel_hi:[1,0,0] neg_lo:[1,0,0] neg_hi:[1,0,0]
	v_pk_fma_f16 v7, v3, v122, v123 op_sel:[0,0,0] op_sel_hi:[1,0,0] neg_lo:[1,0,0] neg_hi:[1,0,0]
	v_pk_fma_f16 v8, v4, v122, v123 op_sel:[0,0,0] op_sel_hi:[1,0,0] neg_lo:[1,0,0] neg_hi:[1,0,0]
	v_pk_fma_f16 v9, v5, v122, v123 op_sel:[0,0,0] op_sel_hi:[1,0,0] neg_lo:[1,0,0] neg_hi:[1,0,0]
	v_mfma_f32_16x16x32_f16 v[22:25], v[10:13], v[2:5], 0
	ds_read2_b64 v[68:71], v32 offset0:5 offset1:207
	v_pk_fma_f16 v2, v52, v6, v2
	v_pk_fma_f16 v3, v53, v7, v3
	v_pk_fma_f16 v4, v54, v8, v4
	v_pk_fma_f16 v5, v55, v9, v5
	v_cndmask_b32_e64 v26, v26, v18, s[60:61]
	s_waitcnt lgkmcnt(10)
	v_pk_fma_f16 v6, v2, v124, v125 op_sel:[0,0,0] op_sel_hi:[1,0,0] neg_lo:[1,0,0] neg_hi:[1,0,0]
	v_pk_fma_f16 v7, v3, v124, v125 op_sel:[0,0,0] op_sel_hi:[1,0,0] neg_lo:[1,0,0] neg_hi:[1,0,0]
	v_pk_fma_f16 v8, v4, v124, v125 op_sel:[0,0,0] op_sel_hi:[1,0,0] neg_lo:[1,0,0] neg_hi:[1,0,0]
	v_pk_fma_f16 v9, v5, v124, v125 op_sel:[0,0,0] op_sel_hi:[1,0,0] neg_lo:[1,0,0] neg_hi:[1,0,0]
	v_mfma_f32_16x16x32_f16 v[18:21], v[10:13], v[2:5], 0
	ds_read2_b64 v[72:75], v32 offset0:6 offset1:208
	ds_read_b128 v[132:135], v33 offset:48
	v_pk_fma_f16 v2, v56, v6, v2
	v_pk_fma_f16 v3, v57, v7, v3
	v_pk_fma_f16 v4, v58, v8, v4
	v_pk_fma_f16 v5, v59, v9, v5
	v_cndmask_b32_e64 v27, v27, v23, s[60:61]
	v_pk_fma_f16 v6, v2, v126, v127 op_sel:[0,0,0] op_sel_hi:[1,0,0] neg_lo:[1,0,0] neg_hi:[1,0,0]
	v_pk_fma_f16 v7, v3, v126, v127 op_sel:[0,0,0] op_sel_hi:[1,0,0] neg_lo:[1,0,0] neg_hi:[1,0,0]
	v_pk_fma_f16 v8, v4, v126, v127 op_sel:[0,0,0] op_sel_hi:[1,0,0] neg_lo:[1,0,0] neg_hi:[1,0,0]
	v_pk_fma_f16 v9, v5, v126, v127 op_sel:[0,0,0] op_sel_hi:[1,0,0] neg_lo:[1,0,0] neg_hi:[1,0,0]
	v_mfma_f32_16x16x32_f16 v[22:25], v[10:13], v[2:5], 0
	ds_read2_b64 v[76:79], v32 offset0:7 offset1:209
	v_pk_fma_f16 v2, v60, v6, v2
	v_pk_fma_f16 v3, v61, v7, v3
	v_pk_fma_f16 v4, v62, v8, v4
	v_pk_fma_f16 v5, v63, v9, v5
	v_cndmask_b32_e64 v28, v28, v20, s[60:61]
	s_waitcnt lgkmcnt(3)
	v_pk_fma_f16 v6, v2, v128, v129 op_sel:[0,0,0] op_sel_hi:[1,0,0] neg_lo:[1,0,0] neg_hi:[1,0,0]
	v_pk_fma_f16 v7, v3, v128, v129 op_sel:[0,0,0] op_sel_hi:[1,0,0] neg_lo:[1,0,0] neg_hi:[1,0,0]
	v_pk_fma_f16 v8, v4, v128, v129 op_sel:[0,0,0] op_sel_hi:[1,0,0] neg_lo:[1,0,0] neg_hi:[1,0,0]
	v_pk_fma_f16 v9, v5, v128, v129 op_sel:[0,0,0] op_sel_hi:[1,0,0] neg_lo:[1,0,0] neg_hi:[1,0,0]
	v_mfma_f32_16x16x32_f16 v[18:21], v[10:13], v[2:5], 0
	ds_read2_b64 v[80:83], v32 offset0:8 offset1:210
	ds_read_b128 v[136:139], v33 offset:64
	v_pk_fma_f16 v2, v64, v6, v2
	v_pk_fma_f16 v3, v65, v7, v3
	v_pk_fma_f16 v4, v66, v8, v4
	v_pk_fma_f16 v5, v67, v9, v5
	v_cndmask_b32_e64 v29, v29, v25, s[60:61]
	v_pk_fma_f16 v6, v2, v130, v131 op_sel:[0,0,0] op_sel_hi:[1,0,0] neg_lo:[1,0,0] neg_hi:[1,0,0]
	v_pk_fma_f16 v7, v3, v130, v131 op_sel:[0,0,0] op_sel_hi:[1,0,0] neg_lo:[1,0,0] neg_hi:[1,0,0]
	v_pk_fma_f16 v8, v4, v130, v131 op_sel:[0,0,0] op_sel_hi:[1,0,0] neg_lo:[1,0,0] neg_hi:[1,0,0]
	v_pk_fma_f16 v9, v5, v130, v131 op_sel:[0,0,0] op_sel_hi:[1,0,0] neg_lo:[1,0,0] neg_hi:[1,0,0]
	v_mfma_f32_16x16x32_f16 v[22:25], v[10:13], v[2:5], 0
	ds_read2_b64 v[84:87], v32 offset0:9 offset1:211
	v_pk_fma_f16 v2, v68, v6, v2
	v_pk_fma_f16 v3, v69, v7, v3
	v_pk_fma_f16 v4, v70, v8, v4
	v_pk_fma_f16 v5, v71, v9, v5
	v_cndmask_b32_e64 v26, v26, v18, s[62:63]
	s_waitcnt lgkmcnt(3)
	v_pk_fma_f16 v6, v2, v132, v133 op_sel:[0,0,0] op_sel_hi:[1,0,0] neg_lo:[1,0,0] neg_hi:[1,0,0]
	v_pk_fma_f16 v7, v3, v132, v133 op_sel:[0,0,0] op_sel_hi:[1,0,0] neg_lo:[1,0,0] neg_hi:[1,0,0]
	v_pk_fma_f16 v8, v4, v132, v133 op_sel:[0,0,0] op_sel_hi:[1,0,0] neg_lo:[1,0,0] neg_hi:[1,0,0]
	v_pk_fma_f16 v9, v5, v132, v133 op_sel:[0,0,0] op_sel_hi:[1,0,0] neg_lo:[1,0,0] neg_hi:[1,0,0]
	v_mfma_f32_16x16x32_f16 v[18:21], v[10:13], v[2:5], 0
	ds_read2_b64 v[88:91], v32 offset0:10 offset1:212
	ds_read_b128 v[140:143], v33 offset:80
	v_pk_fma_f16 v2, v72, v6, v2
	v_pk_fma_f16 v3, v73, v7, v3
	v_pk_fma_f16 v4, v74, v8, v4
	v_pk_fma_f16 v5, v75, v9, v5
	v_cndmask_b32_e64 v27, v27, v23, s[62:63]
	v_pk_fma_f16 v6, v2, v134, v135 op_sel:[0,0,0] op_sel_hi:[1,0,0] neg_lo:[1,0,0] neg_hi:[1,0,0]
	v_pk_fma_f16 v7, v3, v134, v135 op_sel:[0,0,0] op_sel_hi:[1,0,0] neg_lo:[1,0,0] neg_hi:[1,0,0]
	v_pk_fma_f16 v8, v4, v134, v135 op_sel:[0,0,0] op_sel_hi:[1,0,0] neg_lo:[1,0,0] neg_hi:[1,0,0]
	v_pk_fma_f16 v9, v5, v134, v135 op_sel:[0,0,0] op_sel_hi:[1,0,0] neg_lo:[1,0,0] neg_hi:[1,0,0]
	v_mfma_f32_16x16x32_f16 v[22:25], v[10:13], v[2:5], 0
	ds_read2_b64 v[92:95], v32 offset0:11 offset1:213
	v_pk_fma_f16 v2, v76, v6, v2
	v_pk_fma_f16 v3, v77, v7, v3
	v_pk_fma_f16 v4, v78, v8, v4
	v_pk_fma_f16 v5, v79, v9, v5
	v_cndmask_b32_e64 v28, v28, v20, s[62:63]
	s_waitcnt lgkmcnt(3)
	v_pk_fma_f16 v6, v2, v136, v137 op_sel:[0,0,0] op_sel_hi:[1,0,0] neg_lo:[1,0,0] neg_hi:[1,0,0]
	v_pk_fma_f16 v7, v3, v136, v137 op_sel:[0,0,0] op_sel_hi:[1,0,0] neg_lo:[1,0,0] neg_hi:[1,0,0]
	v_pk_fma_f16 v8, v4, v136, v137 op_sel:[0,0,0] op_sel_hi:[1,0,0] neg_lo:[1,0,0] neg_hi:[1,0,0]
	v_pk_fma_f16 v9, v5, v136, v137 op_sel:[0,0,0] op_sel_hi:[1,0,0] neg_lo:[1,0,0] neg_hi:[1,0,0]
	v_mfma_f32_16x16x32_f16 v[18:21], v[10:13], v[2:5], 0
	ds_read2_b64 v[96:99], v32 offset0:12 offset1:214
	ds_read_b128 v[144:147], v33 offset:96
	v_pk_fma_f16 v2, v80, v6, v2
	v_pk_fma_f16 v3, v81, v7, v3
	v_pk_fma_f16 v4, v82, v8, v4
	v_pk_fma_f16 v5, v83, v9, v5
	v_cndmask_b32_e64 v29, v29, v25, s[62:63]
	v_readfirstlane_b32 s4, v37
	v_readfirstlane_b32 s5, v38
	s_and_b32 s4, s4, s5
	s_cbranch_scc0 .Lc0_slow0
.Lc0_back0:
	v_pk_fma_f16 v6, v2, v138, v139 op_sel:[0,0,0] op_sel_hi:[1,0,0] neg_lo:[1,0,0] neg_hi:[1,0,0]
	v_pk_fma_f16 v7, v3, v138, v139 op_sel:[0,0,0] op_sel_hi:[1,0,0] neg_lo:[1,0,0] neg_hi:[1,0,0]
	v_pk_fma_f16 v8, v4, v138, v139 op_sel:[0,0,0] op_sel_hi:[1,0,0] neg_lo:[1,0,0] neg_hi:[1,0,0]
	v_pk_fma_f16 v9, v5, v138, v139 op_sel:[0,0,0] op_sel_hi:[1,0,0] neg_lo:[1,0,0] neg_hi:[1,0,0]
	v_mfma_f32_16x16x32_f16 v[22:25], v[10:13], v[2:5], 0
	ds_read2_b64 v[100:103], v32 offset0:13 offset1:215
	v_pk_fma_f16 v2, v84, v6, v2
	v_pk_fma_f16 v3, v85, v7, v3
	v_pk_fma_f16 v4, v86, v8, v4
	v_pk_fma_f16 v5, v87, v9, v5
	v_cndmask_b32_e64 v26, v26, v18, s[64:65]
	s_waitcnt lgkmcnt(3)
	v_pk_fma_f16 v6, v2, v140, v141 op_sel:[0,0,0] op_sel_hi:[1,0,0] neg_lo:[1,0,0] neg_hi:[1,0,0]
	v_pk_fma_f16 v7, v3, v140, v141 op_sel:[0,0,0] op_sel_hi:[1,0,0] neg_lo:[1,0,0] neg_hi:[1,0,0]
	v_pk_fma_f16 v8, v4, v140, v141 op_sel:[0,0,0] op_sel_hi:[1,0,0] neg_lo:[1,0,0] neg_hi:[1,0,0]
	v_pk_fma_f16 v9, v5, v140, v141 op_sel:[0,0,0] op_sel_hi:[1,0,0] neg_lo:[1,0,0] neg_hi:[1,0,0]
	v_mfma_f32_16x16x32_f16 v[18:21], v[10:13], v[2:5], 0
	ds_read2_b64 v[104:107], v32 offset0:14 offset1:216
	ds_read_b128 v[148:151], v33 offset:112
	v_pk_fma_f16 v2, v88, v6, v2
	v_pk_fma_f16 v3, v89, v7, v3
	v_pk_fma_f16 v4, v90, v8, v4
	v_pk_fma_f16 v5, v91, v9, v5
	v_cndmask_b32_e64 v27, v27, v23, s[64:65]
	v_pk_fma_f16 v6, v2, v142, v143 op_sel:[0,0,0] op_sel_hi:[1,0,0] neg_lo:[1,0,0] neg_hi:[1,0,0]
	v_pk_fma_f16 v7, v3, v142, v143 op_sel:[0,0,0] op_sel_hi:[1,0,0] neg_lo:[1,0,0] neg_hi:[1,0,0]
	v_pk_fma_f16 v8, v4, v142, v143 op_sel:[0,0,0] op_sel_hi:[1,0,0] neg_lo:[1,0,0] neg_hi:[1,0,0]
	v_pk_fma_f16 v9, v5, v142, v143 op_sel:[0,0,0] op_sel_hi:[1,0,0] neg_lo:[1,0,0] neg_hi:[1,0,0]
	v_mfma_f32_16x16x32_f16 v[22:25], v[10:13], v[2:5], 0
	ds_read2_b64 v[108:111], v32 offset0:15 offset1:217
	v_pk_fma_f16 v2, v92, v6, v2
	v_pk_fma_f16 v3, v93, v7, v3
	v_pk_fma_f16 v4, v94, v8, v4
	v_pk_fma_f16 v5, v95, v9, v5
	v_cndmask_b32_e64 v28, v28, v20, s[64:65]
	s_waitcnt lgkmcnt(3)
	v_pk_fma_f16 v6, v2, v144, v145 op_sel:[0,0,0] op_sel_hi:[1,0,0] neg_lo:[1,0,0] neg_hi:[1,0,0]
	v_pk_fma_f16 v7, v3, v144, v145 op_sel:[0,0,0] op_sel_hi:[1,0,0] neg_lo:[1,0,0] neg_hi:[1,0,0]
	v_pk_fma_f16 v8, v4, v144, v145 op_sel:[0,0,0] op_sel_hi:[1,0,0] neg_lo:[1,0,0] neg_hi:[1,0,0]
	v_pk_fma_f16 v9, v5, v144, v145 op_sel:[0,0,0] op_sel_hi:[1,0,0] neg_lo:[1,0,0] neg_hi:[1,0,0]
	v_mfma_f32_16x16x32_f16 v[18:21], v[10:13], v[2:5], 0
	ds_read2_b64 v[48:51], v32 offset0:16 offset1:218
	ds_read_b128 v[120:123], v33 offset:128
	ds_read2_b64 v[14:17], v34 offset0:16 offset1:218
	v_pk_fma_f16 v2, v96, v6, v2
	v_pk_fma_f16 v3, v97, v7, v3
	v_pk_fma_f16 v4, v98, v8, v4
	v_pk_fma_f16 v5, v99, v9, v5
	v_cndmask_b32_e64 v29, v29, v25, s[64:65]
	v_pk_fma_f16 v6, v2, v146, v147 op_sel:[0,0,0] op_sel_hi:[1,0,0] neg_lo:[1,0,0] neg_hi:[1,0,0]
	v_pk_fma_f16 v7, v3, v146, v147 op_sel:[0,0,0] op_sel_hi:[1,0,0] neg_lo:[1,0,0] neg_hi:[1,0,0]
	v_pk_fma_f16 v8, v4, v146, v147 op_sel:[0,0,0] op_sel_hi:[1,0,0] neg_lo:[1,0,0] neg_hi:[1,0,0]
	v_pk_fma_f16 v9, v5, v146, v147 op_sel:[0,0,0] op_sel_hi:[1,0,0] neg_lo:[1,0,0] neg_hi:[1,0,0]
	v_mfma_f32_16x16x32_f16 v[22:25], v[10:13], v[2:5], 0
	ds_read2_b64 v[52:55], v32 offset0:17 offset1:219
	v_pk_fma_f16 v2, v100, v6, v2
	v_pk_fma_f16 v3, v101, v7, v3
	v_pk_fma_f16 v4, v102, v8, v4
	v_pk_fma_f16 v5, v103, v9, v5
	v_cndmask_b32_e64 v26, v26, v18, s[66:67]
	s_waitcnt lgkmcnt(4)
	v_pk_fma_f16 v6, v2, v148, v149 op_sel:[0,0,0] op_sel_hi:[1,0,0] neg_lo:[1,0,0] neg_hi:[1,0,0]
	v_pk_fma_f16 v7, v3, v148, v149 op_sel:[0,0,0] op_sel_hi:[1,0,0] neg_lo:[1,0,0] neg_hi:[1,0,0]
	v_pk_fma_f16 v8, v4, v148, v149 op_sel:[0,0,0] op_sel_hi:[1,0,0] neg_lo:[1,0,0] neg_hi:[1,0,0]
	v_pk_fma_f16 v9, v5, v148, v149 op_sel:[0,0,0] op_sel_hi:[1,0,0] neg_lo:[1,0,0] neg_hi:[1,0,0]
	v_mfma_f32_16x16x32_f16 v[18:21], v[10:13], v[2:5], 0
	ds_read2_b64 v[56:59], v32 offset0:18 offset1:220
	ds_read_b128 v[124:127], v33 offset:144
	v_pk_fma_f16 v2, v104, v6, v2
	v_pk_fma_f16 v3, v105, v7, v3
	v_pk_fma_f16 v4, v106, v8, v4
	v_pk_fma_f16 v5, v107, v9, v5
	v_cndmask_b32_e64 v27, v27, v23, s[66:67]
	v_pk_fma_f16 v6, v2, v150, v151 op_sel:[0,0,0] op_sel_hi:[1,0,0] neg_lo:[1,0,0] neg_hi:[1,0,0]
	v_pk_fma_f16 v7, v3, v150, v151 op_sel:[0,0,0] op_sel_hi:[1,0,0] neg_lo:[1,0,0] neg_hi:[1,0,0]
	v_pk_fma_f16 v8, v4, v150, v151 op_sel:[0,0,0] op_sel_hi:[1,0,0] neg_lo:[1,0,0] neg_hi:[1,0,0]
	v_pk_fma_f16 v9, v5, v150, v151 op_sel:[0,0,0] op_sel_hi:[1,0,0] neg_lo:[1,0,0] neg_hi:[1,0,0]
	v_mfma_f32_16x16x32_f16 v[22:25], v[10:13], v[2:5], 0
	ds_read2_b64 v[60:63], v32 offset0:19 offset1:221
	v_pk_fma_f16 v2, v108, v6, v2
	v_pk_fma_f16 v3, v109, v7, v3
	v_pk_fma_f16 v4, v110, v8, v4
	v_pk_fma_f16 v5, v111, v9, v5
	v_cndmask_b32_e64 v28, v28, v20, s[66:67]
.Lc0_next0:
	s_waitcnt lgkmcnt(3)
	v_pk_fma_f16 v6, v2, v120, v121 op_sel:[0,0,0] op_sel_hi:[1,0,0] neg_lo:[1,0,0] neg_hi:[1,0,0]
	v_pk_fma_f16 v7, v3, v120, v121 op_sel:[0,0,0] op_sel_hi:[1,0,0] neg_lo:[1,0,0] neg_hi:[1,0,0]
	v_pk_fma_f16 v8, v4, v120, v121 op_sel:[0,0,0] op_sel_hi:[1,0,0] neg_lo:[1,0,0] neg_hi:[1,0,0]
	v_pk_fma_f16 v9, v5, v120, v121 op_sel:[0,0,0] op_sel_hi:[1,0,0] neg_lo:[1,0,0] neg_hi:[1,0,0]
	v_mfma_f32_16x16x32_f16 v[18:21], v[14:17], v[2:5], 0
	ds_read2_b64 v[64:67], v32 offset0:20 offset1:222
	ds_read_b128 v[128:131], v33 offset:160
	ds_read_b32 v37, v36 offset:8
	ds_read_b32 v38, v36 offset:72
	v_pk_fma_f16 v2, v48, v6, v2
	v_pk_fma_f16 v3, v49, v7, v3
	v_pk_fma_f16 v4, v50, v8, v4
	v_pk_fma_f16 v5, v51, v9, v5
	v_cndmask_b32_e64 v29, v29, v25, s[66:67]
	v_cvt_pk_f16_f32 v30, v26, v27
	v_cvt_pk_f16_f32 v31, v28, v29
	ds_write_b16 v39, v30 offset:2048
	ds_write_b16_d16_hi v39, v30 offset:2112
	ds_write_b16 v39, v31 offset:2176
	ds_write_b16_d16_hi v39, v31 offset:2240
	s_mov_b64 exec, 1
	ds_add_u32 v36, v44 offset:128
	s_mov_b64 exec, -1
	v_pk_fma_f16 v6, v2, v122, v123 op_sel:[0,0,0] op_sel_hi:[1,0,0] neg_lo:[1,0,0] neg_hi:[1,0,0]
	v_pk_fma_f16 v7, v3, v122, v123 op_sel:[0,0,0] op_sel_hi:[1,0,0] neg_lo:[1,0,0] neg_hi:[1,0,0]
	v_pk_fma_f16 v8, v4, v122, v123 op_sel:[0,0,0] op_sel_hi:[1,0,0] neg_lo:[1,0,0] neg_hi:[1,0,0]
	v_pk_fma_f16 v9, v5, v122, v123 op_sel:[0,0,0] op_sel_hi:[1,0,0] neg_lo:[1,0,0] neg_hi:[1,0,0]
	v_mfma_f32_16x16x32_f16 v[22:25], v[14:17], v[2:5], 0
	ds_read2_b64 v[68:71], v32 offset0:21 offset1:223
	v_pk_fma_f16 v2, v52, v6, v2
	v_pk_fma_f16 v3, v53, v7, v3
	v_pk_fma_f16 v4, v54, v8, v4
	v_pk_fma_f16 v5, v55, v9, v5
	v_cndmask_b32_e64 v26, v26, v18, s[60:61]
	s_waitcnt lgkmcnt(10)
	v_pk_fma_f16 v6, v2, v124, v125 op_sel:[0,0,0] op_sel_hi:[1,0,0] neg_lo:[1,0,0] neg_hi:[1,0,0]
	v_pk_fma_f16 v7, v3, v124, v125 op_sel:[0,0,0] op_sel_hi:[1,0,0] neg_lo:[1,0,0] neg_hi:[1,0,0]
	v_pk_fma_f16 v8, v4, v124, v125 op_sel:[0,0,0] op_sel_hi:[1,0,0] neg_lo:[1,0,0] neg_hi:[1,0,0]
	v_pk_fma_f16 v9, v5, v124, v125 op_sel:[0,0,0] op_sel_hi:[1,0,0] neg_lo:[1,0,0] neg_hi:[1,0,0]
	v_mfma_f32_16x16x32_f16 v[18:21], v[14:17], v[2:5], 0
	ds_read2_b64 v[72:75], v32 offset0:22 offset1:224
	ds_read_b128 v[132:135], v33 offset:176
	v_pk_fma_f16 v2, v56, v6, v2
	v_pk_fma_f16 v3, v57, v7, v3
	v_pk_fma_f16 v4, v58, v8, v4
	v_pk_fma_f16 v5, v59, v9, v5
	v_cndmask_b32_e64 v27, v27, v23, s[60:61]
	v_pk_fma_f16 v6, v2, v126, v127 op_sel:[0,0,0] op_sel_hi:[1,0,0] neg_lo:[1,0,0] neg_hi:[1,0,0]
	v_pk_fma_f16 v7, v3, v126, v127 op_sel:[0,0,0] op_sel_hi:[1,0,0] neg_lo:[1,0,0] neg_hi:[1,0,0]
	v_pk_fma_f16 v8, v4, v126, v127 op_sel:[0,0,0] op_sel_hi:[1,0,0] neg_lo:[1,0,0] neg_hi:[1,0,0]
	v_pk_fma_f16 v9, v5, v126, v127 op_sel:[0,0,0] op_sel_hi:[1,0,0] neg_lo:[1,0,0] neg_hi:[1,0,0]
	v_mfma_f32_16x16x32_f16 v[22:25], v[14:17], v[2:5], 0
	ds_read2_b64 v[76:79], v32 offset0:23 offset1:225
	v_pk_fma_f16 v2, v60, v6, v2
	v_pk_fma_f16 v3, v61, v7, v3
	v_pk_fma_f16 v4, v62, v8, v4
	v_pk_fma_f16 v5, v63, v9, v5
	v_cndmask_b32_e64 v28, v28, v20, s[60:61]
	s_waitcnt lgkmcnt(3)
	v_pk_fma_f16 v6, v2, v128, v129 op_sel:[0,0,0] op_sel_hi:[1,0,0] neg_lo:[1,0,0] neg_hi:[1,0,0]
	v_pk_fma_f16 v7, v3, v128, v129 op_sel:[0,0,0] op_sel_hi:[1,0,0] neg_lo:[1,0,0] neg_hi:[1,0,0]
	v_pk_fma_f16 v8, v4, v128, v129 op_sel:[0,0,0] op_sel_hi:[1,0,0] neg_lo:[1,0,0] neg_hi:[1,0,0]
	v_pk_fma_f16 v9, v5, v128, v129 op_sel:[0,0,0] op_sel_hi:[1,0,0] neg_lo:[1,0,0] neg_hi:[1,0,0]
	v_mfma_f32_16x16x32_f16 v[18:21], v[14:17], v[2:5], 0
	ds_read2_b64 v[80:83], v32 offset0:24 offset1:226
	ds_read_b128 v[136:139], v33 offset:192
	v_pk_fma_f16 v2, v64, v6, v2
	v_pk_fma_f16 v3, v65, v7, v3
	v_pk_fma_f16 v4, v66, v8, v4
	v_pk_fma_f16 v5, v67, v9, v5
	v_cndmask_b32_e64 v29, v29, v25, s[60:61]
	v_pk_fma_f16 v6, v2, v130, v131 op_sel:[0,0,0] op_sel_hi:[1,0,0] neg_lo:[1,0,0] neg_hi:[1,0,0]
	v_pk_fma_f16 v7, v3, v130, v131 op_sel:[0,0,0] op_sel_hi:[1,0,0] neg_lo:[1,0,0] neg_hi:[1,0,0]
	v_pk_fma_f16 v8, v4, v130, v131 op_sel:[0,0,0] op_sel_hi:[1,0,0] neg_lo:[1,0,0] neg_hi:[1,0,0]
	v_pk_fma_f16 v9, v5, v130, v131 op_sel:[0,0,0] op_sel_hi:[1,0,0] neg_lo:[1,0,0] neg_hi:[1,0,0]
	v_mfma_f32_16x16x32_f16 v[22:25], v[14:17], v[2:5], 0
	ds_read2_b64 v[84:87], v32 offset0:25 offset1:227
	v_pk_fma_f16 v2, v68, v6, v2
	v_pk_fma_f16 v3, v69, v7, v3
	v_pk_fma_f16 v4, v70, v8, v4
	v_pk_fma_f16 v5, v71, v9, v5
	v_cndmask_b32_e64 v26, v26, v18, s[62:63]
	s_waitcnt lgkmcnt(3)
	v_pk_fma_f16 v6, v2, v132, v133 op_sel:[0,0,0] op_sel_hi:[1,0,0] neg_lo:[1,0,0] neg_hi:[1,0,0]
	v_pk_fma_f16 v7, v3, v132, v133 op_sel:[0,0,0] op_sel_hi:[1,0,0] neg_lo:[1,0,0] neg_hi:[1,0,0]
	v_pk_fma_f16 v8, v4, v132, v133 op_sel:[0,0,0] op_sel_hi:[1,0,0] neg_lo:[1,0,0] neg_hi:[1,0,0]
	v_pk_fma_f16 v9, v5, v132, v133 op_sel:[0,0,0] op_sel_hi:[1,0,0] neg_lo:[1,0,0] neg_hi:[1,0,0]
	v_mfma_f32_16x16x32_f16 v[18:21], v[14:17], v[2:5], 0
	ds_read2_b64 v[88:91], v32 offset0:26 offset1:228
	ds_read_b128 v[140:143], v33 offset:208
	v_pk_fma_f16 v2, v72, v6, v2
	v_pk_fma_f16 v3, v73, v7, v3
	v_pk_fma_f16 v4, v74, v8, v4
	v_pk_fma_f16 v5, v75, v9, v5
	v_cndmask_b32_e64 v27, v27, v23, s[62:63]
	v_pk_fma_f16 v6, v2, v134, v135 op_sel:[0,0,0] op_sel_hi:[1,0,0] neg_lo:[1,0,0] neg_hi:[1,0,0]
	v_pk_fma_f16 v7, v3, v134, v135 op_sel:[0,0,0] op_sel_hi:[1,0,0] neg_lo:[1,0,0] neg_hi:[1,0,0]
	v_pk_fma_f16 v8, v4, v134, v135 op_sel:[0,0,0] op_sel_hi:[1,0,0] neg_lo:[1,0,0] neg_hi:[1,0,0]
	v_pk_fma_f16 v9, v5, v134, v135 op_sel:[0,0,0] op_sel_hi:[1,0,0] neg_lo:[1,0,0] neg_hi:[1,0,0]
	v_mfma_f32_16x16x32_f16 v[22:25], v[14:17], v[2:5], 0
	ds_read2_b64 v[92:95], v32 offset0:27 offset1:229
	v_pk_fma_f16 v2, v76, v6, v2
	v_pk_fma_f16 v3, v77, v7, v3
	v_pk_fma_f16 v4, v78, v8, v4
	v_pk_fma_f16 v5, v79, v9, v5
	v_cndmask_b32_e64 v28, v28, v20, s[62:63]
	s_waitcnt lgkmcnt(3)
	v_pk_fma_f16 v6, v2, v136, v137 op_sel:[0,0,0] op_sel_hi:[1,0,0] neg_lo:[1,0,0] neg_hi:[1,0,0]
	v_pk_fma_f16 v7, v3, v136, v137 op_sel:[0,0,0] op_sel_hi:[1,0,0] neg_lo:[1,0,0] neg_hi:[1,0,0]
	v_pk_fma_f16 v8, v4, v136, v137 op_sel:[0,0,0] op_sel_hi:[1,0,0] neg_lo:[1,0,0] neg_hi:[1,0,0]
	v_pk_fma_f16 v9, v5, v136, v137 op_sel:[0,0,0] op_sel_hi:[1,0,0] neg_lo:[1,0,0] neg_hi:[1,0,0]
	v_mfma_f32_16x16x32_f16 v[18:21], v[14:17], v[2:5], 0
	ds_read2_b64 v[96:99], v32 offset0:28 offset1:230
	ds_read_b128 v[144:147], v33 offset:224
	v_pk_fma_f16 v2, v80, v6, v2
	v_pk_fma_f16 v3, v81, v7, v3
	v_pk_fma_f16 v4, v82, v8, v4
	v_pk_fma_f16 v5, v83, v9, v5
	v_cndmask_b32_e64 v29, v29, v25, s[62:63]
	v_readfirstlane_b32 s4, v37
	v_readfirstlane_b32 s5, v38
	s_and_b32 s4, s4, s5
	s_cbranch_scc0 .Lc0_slow1
.Lc0_back1:
	v_pk_fma_f16 v6, v2, v138, v139 op_sel:[0,0,0] op_sel_hi:[1,0,0] neg_lo:[1,0,0] neg_hi:[1,0,0]
	v_pk_fma_f16 v7, v3, v138, v139 op_sel:[0,0,0] op_sel_hi:[1,0,0] neg_lo:[1,0,0] neg_hi:[1,0,0]
	v_pk_fma_f16 v8, v4, v138, v139 op_sel:[0,0,0] op_sel_hi:[1,0,0] neg_lo:[1,0,0] neg_hi:[1,0,0]
	v_pk_fma_f16 v9, v5, v138, v139 op_sel:[0,0,0] op_sel_hi:[1,0,0] neg_lo:[1,0,0] neg_hi:[1,0,0]
	v_mfma_f32_16x16x32_f16 v[22:25], v[14:17], v[2:5], 0
	ds_read2_b64 v[100:103], v32 offset0:29 offset1:231
	v_pk_fma_f16 v2, v84, v6, v2
	v_pk_fma_f16 v3, v85, v7, v3
	v_pk_fma_f16 v4, v86, v8, v4
	v_pk_fma_f16 v5, v87, v9, v5
	v_cndmask_b32_e64 v26, v26, v18, s[64:65]
	s_waitcnt lgkmcnt(3)
	v_pk_fma_f16 v6, v2, v140, v141 op_sel:[0,0,0] op_sel_hi:[1,0,0] neg_lo:[1,0,0] neg_hi:[1,0,0]
	v_pk_fma_f16 v7, v3, v140, v141 op_sel:[0,0,0] op_sel_hi:[1,0,0] neg_lo:[1,0,0] neg_hi:[1,0,0]
	v_pk_fma_f16 v8, v4, v140, v141 op_sel:[0,0,0] op_sel_hi:[1,0,0] neg_lo:[1,0,0] neg_hi:[1,0,0]
	v_pk_fma_f16 v9, v5, v140, v141 op_sel:[0,0,0] op_sel_hi:[1,0,0] neg_lo:[1,0,0] neg_hi:[1,0,0]
	v_mfma_f32_16x16x32_f16 v[18:21], v[14:17], v[2:5], 0
	ds_read2_b64 v[104:107], v32 offset0:30 offset1:232
	ds_read_b128 v[148:151], v33 offset:240
	v_pk_fma_f16 v2, v88, v6, v2
	v_pk_fma_f16 v3, v89, v7, v3
	v_pk_fma_f16 v4, v90, v8, v4
	v_pk_fma_f16 v5, v91, v9, v5
	v_cndmask_b32_e64 v27, v27, v23, s[64:65]
	v_pk_fma_f16 v6, v2, v142, v143 op_sel:[0,0,0] op_sel_hi:[1,0,0] neg_lo:[1,0,0] neg_hi:[1,0,0]
	v_pk_fma_f16 v7, v3, v142, v143 op_sel:[0,0,0] op_sel_hi:[1,0,0] neg_lo:[1,0,0] neg_hi:[1,0,0]
	v_pk_fma_f16 v8, v4, v142, v143 op_sel:[0,0,0] op_sel_hi:[1,0,0] neg_lo:[1,0,0] neg_hi:[1,0,0]
	v_pk_fma_f16 v9, v5, v142, v143 op_sel:[0,0,0] op_sel_hi:[1,0,0] neg_lo:[1,0,0] neg_hi:[1,0,0]
	v_mfma_f32_16x16x32_f16 v[22:25], v[14:17], v[2:5], 0
	ds_read2_b64 v[108:111], v32 offset0:31 offset1:233
	v_pk_fma_f16 v2, v92, v6, v2
	v_pk_fma_f16 v3, v93, v7, v3
	v_pk_fma_f16 v4, v94, v8, v4
	v_pk_fma_f16 v5, v95, v9, v5
	v_cndmask_b32_e64 v28, v28, v20, s[64:65]
	s_waitcnt lgkmcnt(3)
	v_pk_fma_f16 v6, v2, v144, v145 op_sel:[0,0,0] op_sel_hi:[1,0,0] neg_lo:[1,0,0] neg_hi:[1,0,0]
	v_pk_fma_f16 v7, v3, v144, v145 op_sel:[0,0,0] op_sel_hi:[1,0,0] neg_lo:[1,0,0] neg_hi:[1,0,0]
	v_pk_fma_f16 v8, v4, v144, v145 op_sel:[0,0,0] op_sel_hi:[1,0,0] neg_lo:[1,0,0] neg_hi:[1,0,0]
	v_pk_fma_f16 v9, v5, v144, v145 op_sel:[0,0,0] op_sel_hi:[1,0,0] neg_lo:[1,0,0] neg_hi:[1,0,0]
	v_mfma_f32_16x16x32_f16 v[18:21], v[14:17], v[2:5], 0
	ds_read2_b64 v[48:51], v32 offset0:32 offset1:234
	ds_read_b128 v[120:123], v33 offset:256
	ds_read2_b64 v[10:13], v34 offset0:32 offset1:234
	v_pk_fma_f16 v2, v96, v6, v2
	v_pk_fma_f16 v3, v97, v7, v3
	v_pk_fma_f16 v4, v98, v8, v4
	v_pk_fma_f16 v5, v99, v9, v5
	v_cndmask_b32_e64 v29, v29, v25, s[64:65]
	v_pk_fma_f16 v6, v2, v146, v147 op_sel:[0,0,0] op_sel_hi:[1,0,0] neg_lo:[1,0,0] neg_hi:[1,0,0]
	v_pk_fma_f16 v7, v3, v146, v147 op_sel:[0,0,0] op_sel_hi:[1,0,0] neg_lo:[1,0,0] neg_hi:[1,0,0]
	v_pk_fma_f16 v8, v4, v146, v147 op_sel:[0,0,0] op_sel_hi:[1,0,0] neg_lo:[1,0,0] neg_hi:[1,0,0]
	v_pk_fma_f16 v9, v5, v146, v147 op_sel:[0,0,0] op_sel_hi:[1,0,0] neg_lo:[1,0,0] neg_hi:[1,0,0]
	v_mfma_f32_16x16x32_f16 v[22:25], v[14:17], v[2:5], 0
	ds_read2_b64 v[52:55], v32 offset0:33 offset1:235
	v_pk_fma_f16 v2, v100, v6, v2
	v_pk_fma_f16 v3, v101, v7, v3
	v_pk_fma_f16 v4, v102, v8, v4
	v_pk_fma_f16 v5, v103, v9, v5
	v_cndmask_b32_e64 v26, v26, v18, s[66:67]
	s_waitcnt lgkmcnt(4)
	v_pk_fma_f16 v6, v2, v148, v149 op_sel:[0,0,0] op_sel_hi:[1,0,0] neg_lo:[1,0,0] neg_hi:[1,0,0]
	v_pk_fma_f16 v7, v3, v148, v149 op_sel:[0,0,0] op_sel_hi:[1,0,0] neg_lo:[1,0,0] neg_hi:[1,0,0]
	v_pk_fma_f16 v8, v4, v148, v149 op_sel:[0,0,0] op_sel_hi:[1,0,0] neg_lo:[1,0,0] neg_hi:[1,0,0]
	v_pk_fma_f16 v9, v5, v148, v149 op_sel:[0,0,0] op_sel_hi:[1,0,0] neg_lo:[1,0,0] neg_hi:[1,0,0]
	v_mfma_f32_16x16x32_f16 v[18:21], v[14:17], v[2:5], 0
	ds_read2_b64 v[56:59], v32 offset0:34 offset1:236
	ds_read_b128 v[124:127], v33 offset:272
	v_pk_fma_f16 v2, v104, v6, v2
	v_pk_fma_f16 v3, v105, v7, v3
	v_pk_fma_f16 v4, v106, v8, v4
	v_pk_fma_f16 v5, v107, v9, v5
	v_cndmask_b32_e64 v27, v27, v23, s[66:67]
	v_pk_fma_f16 v6, v2, v150, v151 op_sel:[0,0,0] op_sel_hi:[1,0,0] neg_lo:[1,0,0] neg_hi:[1,0,0]
	v_pk_fma_f16 v7, v3, v150, v151 op_sel:[0,0,0] op_sel_hi:[1,0,0] neg_lo:[1,0,0] neg_hi:[1,0,0]
	v_pk_fma_f16 v8, v4, v150, v151 op_sel:[0,0,0] op_sel_hi:[1,0,0] neg_lo:[1,0,0] neg_hi:[1,0,0]
	v_pk_fma_f16 v9, v5, v150, v151 op_sel:[0,0,0] op_sel_hi:[1,0,0] neg_lo:[1,0,0] neg_hi:[1,0,0]
	v_mfma_f32_16x16x32_f16 v[22:25], v[14:17], v[2:5], 0
	ds_read2_b64 v[60:63], v32 offset0:35 offset1:237
	v_pk_fma_f16 v2, v108, v6, v2
	v_pk_fma_f16 v3, v109, v7, v3
	v_pk_fma_f16 v4, v110, v8, v4
	v_pk_fma_f16 v5, v111, v9, v5
	v_cndmask_b32_e64 v28, v28, v20, s[66:67]
.Lc0_next1:
	v_add_u32_e32 v32, 0x100, v32
	v_add_u32_e32 v33, 0x100, v33
	v_add_u32_e32 v34, 0x100, v34
	v_add_u32_e32 v36, 8, v36
	v_add_u32_e32 v39, 0x1000, v39
	v_add_u32_e32 v43, 0x1000, v43
	v_add_u32_e32 v35, 0x800, v35
	s_xor_b32 s71, s71, 2
	s_add_i32 s70, s70, 1
	s_cmp_lt_u32 s70, 6
	s_cbranch_scc1 .Lc0_loop
	s_waitcnt lgkmcnt(3)
	v_pk_fma_f16 v6, v2, v120, v121 op_sel:[0,0,0] op_sel_hi:[1,0,0] neg_lo:[1,0,0] neg_hi:[1,0,0]
	v_pk_fma_f16 v7, v3, v120, v121 op_sel:[0,0,0] op_sel_hi:[1,0,0] neg_lo:[1,0,0] neg_hi:[1,0,0]
	v_pk_fma_f16 v8, v4, v120, v121 op_sel:[0,0,0] op_sel_hi:[1,0,0] neg_lo:[1,0,0] neg_hi:[1,0,0]
	v_pk_fma_f16 v9, v5, v120, v121 op_sel:[0,0,0] op_sel_hi:[1,0,0] neg_lo:[1,0,0] neg_hi:[1,0,0]
	v_mfma_f32_16x16x32_f16 v[18:21], v[10:13], v[2:5], 0
	ds_read2_b64 v[64:67], v32 offset0:4 offset1:206
	ds_read_b128 v[128:131], v33 offset:32
	v_pk_fma_f16 v2, v48, v6, v2
	v_pk_fma_f16 v3, v49, v7, v3
	v_pk_fma_f16 v4, v50, v8, v4
	v_pk_fma_f16 v5, v51, v9, v5
	v_cndmask_b32_e64 v29, v29, v25, s[66:67]
	v_cvt_pk_f16_f32 v30, v26, v27
	v_cvt_pk_f16_f32 v31, v28, v29
	ds_write_b16 v39, v30 offset:0
	ds_write_b16_d16_hi v39, v30 offset:64
	ds_write_b16 v39, v31 offset:128
	ds_write_b16_d16_hi v39, v31 offset:192
	s_mov_b64 exec, 1
	ds_add_u32 v36, v44 offset:124
	s_mov_b64 exec, -1
	v_pk_fma_f16 v6, v2, v122, v123 op_sel:[0,0,0] op_sel_hi:[1,0,0] neg_lo:[1,0,0] neg_hi:[1,0,0]
	v_pk_fma_f16 v7, v3, v122, v123 op_sel:[0,0,0] op_sel_hi:[1,0,0] neg_lo:[1,0,0] neg_hi:[1,0,0]
	v_pk_fma_f16 v8, v4, v122, v123 op_sel:[0,0,0] op_sel_hi:[1,0,0] neg_lo:[1,0,0] neg_hi:[1,0,0]
	v_pk_fma_f16 v9, v5, v122, v123 op_sel:[0,0,0] op_sel_hi:[1,0,0] neg_lo:[1,0,0] neg_hi:[1,0,0]
	v_mfma_f32_16x16x32_f16 v[22:25], v[10:13], v[2:5], 0
	ds_read2_b64 v[68:71], v32 offset0:5 offset1:207
	v_pk_fma_f16 v2, v52, v6, v2
	v_pk_fma_f16 v3, v53, v7, v3
	v_pk_fma_f16 v4, v54, v8, v4
	v_pk_fma_f16 v5, v55, v9, v5
	v_cndmask_b32_e64 v26, v26, v18, s[60:61]
	s_waitcnt lgkmcnt(8)
	v_pk_fma_f16 v6, v2, v124, v125 op_sel:[0,0,0] op_sel_hi:[1,0,0] neg_lo:[1,0,0] neg_hi:[1,0,0]
	v_pk_fma_f16 v7, v3, v124, v125 op_sel:[0,0,0] op_sel_hi:[1,0,0] neg_lo:[1,0,0] neg_hi:[1,0,0]
	v_pk_fma_f16 v8, v4, v124, v125 op_sel:[0,0,0] op_sel_hi:[1,0,0] neg_lo:[1,0,0] neg_hi:[1,0,0]
	v_pk_fma_f16 v9, v5, v124, v125 op_sel:[0,0,0] op_sel_hi:[1,0,0] neg_lo:[1,0,0] neg_hi:[1,0,0]
	v_mfma_f32_16x16x32_f16 v[18:21], v[10:13], v[2:5], 0
	ds_read2_b64 v[72:75], v32 offset0:6 offset1:208
	ds_read_b128 v[132:135], v33 offset:48
	v_pk_fma_f16 v2, v56, v6, v2
	v_pk_fma_f16 v3, v57, v7, v3
	v_pk_fma_f16 v4, v58, v8, v4
	v_pk_fma_f16 v5, v59, v9, v5
	v_cndmask_b32_e64 v27, v27, v23, s[60:61]
	v_pk_fma_f16 v6, v2, v126, v127 op_sel:[0,0,0] op_sel_hi:[1,0,0] neg_lo:[1,0,0] neg_hi:[1,0,0]
	v_pk_fma_f16 v7, v3, v126, v127 op_sel:[0,0,0] op_sel_hi:[1,0,0] neg_lo:[1,0,0] neg_hi:[1,0,0]
	v_pk_fma_f16 v8, v4, v126, v127 op_sel:[0,0,0] op_sel_hi:[1,0,0] neg_lo:[1,0,0] neg_hi:[1,0,0]
	v_pk_fma_f16 v9, v5, v126, v127 op_sel:[0,0,0] op_sel_hi:[1,0,0] neg_lo:[1,0,0] neg_hi:[1,0,0]
	v_mfma_f32_16x16x32_f16 v[22:25], v[10:13], v[2:5], 0
	ds_read2_b64 v[76:79], v32 offset0:7 offset1:209
	v_pk_fma_f16 v2, v60, v6, v2
	v_pk_fma_f16 v3, v61, v7, v3
	v_pk_fma_f16 v4, v62, v8, v4
	v_pk_fma_f16 v5, v63, v9, v5
	v_cndmask_b32_e64 v28, v28, v20, s[60:61]
	s_waitcnt lgkmcnt(3)
	v_pk_fma_f16 v6, v2, v128, v129 op_sel:[0,0,0] op_sel_hi:[1,0,0] neg_lo:[1,0,0] neg_hi:[1,0,0]
	v_pk_fma_f16 v7, v3, v128, v129 op_sel:[0,0,0] op_sel_hi:[1,0,0] neg_lo:[1,0,0] neg_hi:[1,0,0]
	v_pk_fma_f16 v8, v4, v128, v129 op_sel:[0,0,0] op_sel_hi:[1,0,0] neg_lo:[1,0,0] neg_hi:[1,0,0]
	v_pk_fma_f16 v9, v5, v128, v129 op_sel:[0,0,0] op_sel_hi:[1,0,0] neg_lo:[1,0,0] neg_hi:[1,0,0]
	v_mfma_f32_16x16x32_f16 v[18:21], v[10:13], v[2:5], 0
	v_pk_fma_f16 v2, v64, v6, v2
	v_pk_fma_f16 v3, v65, v7, v3
	v_pk_fma_f16 v4, v66, v8, v4
	v_pk_fma_f16 v5, v67, v9, v5
	v_cndmask_b32_e64 v29, v29, v25, s[60:61]
	v_pk_fma_f16 v6, v2, v130, v131 op_sel:[0,0,0] op_sel_hi:[1,0,0] neg_lo:[1,0,0] neg_hi:[1,0,0]
	v_pk_fma_f16 v7, v3, v130, v131 op_sel:[0,0,0] op_sel_hi:[1,0,0] neg_lo:[1,0,0] neg_hi:[1,0,0]
	v_pk_fma_f16 v8, v4, v130, v131 op_sel:[0,0,0] op_sel_hi:[1,0,0] neg_lo:[1,0,0] neg_hi:[1,0,0]
	v_pk_fma_f16 v9, v5, v130, v131 op_sel:[0,0,0] op_sel_hi:[1,0,0] neg_lo:[1,0,0] neg_hi:[1,0,0]
	v_mfma_f32_16x16x32_f16 v[22:25], v[10:13], v[2:5], 0
	v_pk_fma_f16 v2, v68, v6, v2
	v_pk_fma_f16 v3, v69, v7, v3
	v_pk_fma_f16 v4, v70, v8, v4
	v_pk_fma_f16 v5, v71, v9, v5
	v_cndmask_b32_e64 v26, v26, v18, s[62:63]
	s_waitcnt lgkmcnt(0)
	v_pk_fma_f16 v6, v2, v132, v133 op_sel:[0,0,0] op_sel_hi:[1,0,0] neg_lo:[1,0,0] neg_hi:[1,0,0]
	v_pk_fma_f16 v7, v3, v132, v133 op_sel:[0,0,0] op_sel_hi:[1,0,0] neg_lo:[1,0,0] neg_hi:[1,0,0]
	v_pk_fma_f16 v8, v4, v132, v133 op_sel:[0,0,0] op_sel_hi:[1,0,0] neg_lo:[1,0,0] neg_hi:[1,0,0]
	v_pk_fma_f16 v9, v5, v132, v133 op_sel:[0,0,0] op_sel_hi:[1,0,0] neg_lo:[1,0,0] neg_hi:[1,0,0]
	v_mfma_f32_16x16x32_f16 v[18:21], v[10:13], v[2:5], 0
	v_pk_fma_f16 v2, v72, v6, v2
	v_pk_fma_f16 v3, v73, v7, v3
	v_pk_fma_f16 v4, v74, v8, v4
	v_pk_fma_f16 v5, v75, v9, v5
	v_cndmask_b32_e64 v27, v27, v23, s[62:63]
	v_pk_fma_f16 v6, v2, v134, v135 op_sel:[0,0,0] op_sel_hi:[1,0,0] neg_lo:[1,0,0] neg_hi:[1,0,0]
	v_pk_fma_f16 v7, v3, v134, v135 op_sel:[0,0,0] op_sel_hi:[1,0,0] neg_lo:[1,0,0] neg_hi:[1,0,0]
	v_pk_fma_f16 v8, v4, v134, v135 op_sel:[0,0,0] op_sel_hi:[1,0,0] neg_lo:[1,0,0] neg_hi:[1,0,0]
	v_pk_fma_f16 v9, v5, v134, v135 op_sel:[0,0,0] op_sel_hi:[1,0,0] neg_lo:[1,0,0] neg_hi:[1,0,0]
	v_mfma_f32_16x16x32_f16 v[22:25], v[10:13], v[2:5], 0
	v_pk_fma_f16 v2, v76, v6, v2
	v_pk_fma_f16 v3, v77, v7, v3
	v_pk_fma_f16 v4, v78, v8, v4
	v_pk_fma_f16 v5, v79, v9, v5
	v_cndmask_b32_e64 v28, v28, v20, s[62:63]
	s_nop 7
	v_cndmask_b32_e64 v29, v29, v25, s[62:63]
	v_cvt_pk_f16_f32 v30, v26, v27
	v_cvt_pk_f16_f32 v31, v28, v29
	ds_write_b16 v39, v30 offset:2048
	ds_write_b16_d16_hi v39, v30 offset:2112
	ds_write_b16 v39, v31 offset:2176
	ds_write_b16_d16_hi v39, v31 offset:2240
	s_mov_b64 exec, 1
	ds_add_u32 v36, v44 offset:128
	s_mov_b64 exec, -1
	s_branch .Lc0_end

.Lc_par1:
	ds_read2_b64 v[48:51], v32 offset0:0 offset1:202
	ds_read_b128 v[120:123], v33 offset:0
	ds_read2_b64 v[10:13], v34 offset0:0 offset1:202
	ds_read2_b64 v[52:55], v32 offset0:1 offset1:203
	ds_read2_b64 v[56:59], v32 offset0:2 offset1:204
	ds_read_b128 v[124:127], v33 offset:16
	ds_read2_b64 v[60:63], v32 offset0:3 offset1:205
	s_mov_b32 s70, 0
	s_mov_b32 s71, 0
.Lc1_loop:
	s_waitcnt lgkmcnt(3)
	v_pk_fma_f16 v6, v2, v120, v121 op_sel:[0,1,1] op_sel_hi:[1,1,1] neg_lo:[1,0,0] neg_hi:[1,0,0]
	v_pk_fma_f16 v7, v3, v120, v121 op_sel:[0,1,1] op_sel_hi:[1,1,1] neg_lo:[1,0,0] neg_hi:[1,0,0]
	v_pk_fma_f16 v8, v4, v120, v121 op_sel:[0,1,1] op_sel_hi:[1,1,1] neg_lo:[1,0,0] neg_hi:[1,0,0]
	v_pk_fma_f16 v9, v5, v120, v121 op_sel:[0,1,1] op_sel_hi:[1,1,1] neg_lo:[1,0,0] neg_hi:[1,0,0]
	v_mfma_f32_16x16x32_f16 v[18:21], v[10:13], v[2:5], 0
	ds_read2_b64 v[64:67], v32 offset0:4 offset1:206
	ds_read_b128 v[128:131], v33 offset:32
	ds_read_b32 v37, v36 offset:4
	ds_read_b32 v38, v36 offset:68
	v_pk_fma_f16 v2, v48, v6, v2
	v_pk_fma_f16 v3, v49, v7, v3
	v_pk_fma_f16 v4, v50, v8, v4
	v_pk_fma_f16 v5, v51, v9, v5
	v_cndmask_b32_e64 v29, v29, v25, s[66:67]
	v_cvt_pk_f16_f32 v30, v26, v27
	v_cvt_pk_f16_f32 v31, v28, v29
	ds_write_b16 v39, v30 offset:0
	ds_write_b16_d16_hi v39, v30 offset:64
	ds_write_b16 v39, v31 offset:128
	ds_write_b16_d16_hi v39, v31 offset:192
	s_mov_b64 exec, 1
	ds_add_u32 v36, v44 offset:124
	s_mov_b64 exec, -1
	v_pk_fma_f16 v6, v2, v122, v123 op_sel:[0,1,1] op_sel_hi:[1,1,1] neg_lo:[1,0,0] neg_hi:[1,0,0]
	v_pk_fma_f16 v7, v3, v122, v123 op_sel:[0,1,1] op_sel_hi:[1,1,1] neg_lo:[1,0,0] neg_hi:[1,0,0]
	v_pk_fma_f16 v8, v4, v122, v123 op_sel:[0,1,1] op_sel_hi:[1,1,1] neg_lo:[1,0,0] neg_hi:[1,0,0]
	v_pk_fma_f16 v9, v5, v122, v123 op_sel:[0,1,1] op_sel_hi:[1,1,1] neg_lo:[1,0,0] neg_hi:[1,0,0]
	v_mfma_f32_16x16x32_f16 v[22:25], v[10:13], v[2:5], 0
	ds_read2_b64 v[68:71], v32 offset0:5 offset1:207
	v_pk_fma_f16 v2, v52, v6, v2
	v_pk_fma_f16 v3, v53, v7, v3
	v_pk_fma_f16 v4, v54, v8, v4
	v_pk_fma_f16 v5, v55, v9, v5
	v_cndmask_b32_e64 v26, v26, v18, s[60:61]
	s_waitcnt lgkmcnt(10)
	v_pk_fma_f16 v6, v2, v124, v125 op_sel:[0,1,1] op_sel_hi:[1,1,1] neg_lo:[1,0,0] neg_hi:[1,0,0]
	v_pk_fma_f16 v7, v3, v124, v125 op_sel:[0,1,1] op_sel_hi:[1,1,1] neg_lo:[1,0,0] neg_hi:[1,0,0]
	v_pk_fma_f16 v8, v4, v124, v125 op_sel:[0,1,1] op_sel_hi:[1,1,1] neg_lo:[1,0,0] neg_hi:[1,0,0]
	v_pk_fma_f16 v9, v5, v124, v125 op_sel:[0,1,1] op_sel_hi:[1,1,1] neg_lo:[1,0,0] neg_hi:[1,0,0]
	v_mfma_f32_16x16x32_f16 v[18:21], v[10:13], v[2:5], 0
	ds_read2_b64 v[72:75], v32 offset0:6 offset1:208
	ds_read_b128 v[132:135], v33 offset:48
	v_pk_fma_f16 v2, v56, v6, v2
	v_pk_fma_f16 v3, v57, v7, v3
	v_pk_fma_f16 v4, v58, v8, v4
	v_pk_fma_f16 v5, v59, v9, v5
	v_cndmask_b32_e64 v27, v27, v23, s[60:61]
	v_pk_fma_f16 v6, v2, v126, v127 op_sel:[0,1,1] op_sel_hi:[1,1,1] neg_lo:[1,0,0] neg_hi:[1,0,0]
	v_pk_fma_f16 v7, v3, v126, v127 op_sel:[0,1,1] op_sel_hi:[1,1,1] neg_lo:[1,0,0] neg_hi:[1,0,0]
	v_pk_fma_f16 v8, v4, v126, v127 op_sel:[0,1,1] op_sel_hi:[1,1,1] neg_lo:[1,0,0] neg_hi:[1,0,0]
	v_pk_fma_f16 v9, v5, v126, v127 op_sel:[0,1,1] op_sel_hi:[1,1,1] neg_lo:[1,0,0] neg_hi:[1,0,0]
	v_mfma_f32_16x16x32_f16 v[22:25], v[10:13], v[2:5], 0
	ds_read2_b64 v[76:79], v32 offset0:7 offset1:209
	v_pk_fma_f16 v2, v60, v6, v2
	v_pk_fma_f16 v3, v61, v7, v3
	v_pk_fma_f16 v4, v62, v8, v4
	v_pk_fma_f16 v5, v63, v9, v5
	v_cndmask_b32_e64 v28, v28, v20, s[60:61]
	s_waitcnt lgkmcnt(3)
	v_pk_fma_f16 v6, v2, v128, v129 op_sel:[0,1,1] op_sel_hi:[1,1,1] neg_lo:[1,0,0] neg_hi:[1,0,0]
	v_pk_fma_f16 v7, v3, v128, v129 op_sel:[0,1,1] op_sel_hi:[1,1,1] neg_lo:[1,0,0] neg_hi:[1,0,0]
	v_pk_fma_f16 v8, v4, v128, v129 op_sel:[0,1,1] op_sel_hi:[1,1,1] neg_lo:[1,0,0] neg_hi:[1,0,0]
	v_pk_fma_f16 v9, v5, v128, v129 op_sel:[0,1,1] op_sel_hi:[1,1,1] neg_lo:[1,0,0] neg_hi:[1,0,0]
	v_mfma_f32_16x16x32_f16 v[18:21], v[10:13], v[2:5], 0
	ds_read2_b64 v[80:83], v32 offset0:8 offset1:210
	ds_read_b128 v[136:139], v33 offset:64
	v_pk_fma_f16 v2, v64, v6, v2
	v_pk_fma_f16 v3, v65, v7, v3
	v_pk_fma_f16 v4, v66, v8, v4
	v_pk_fma_f16 v5, v67, v9, v5
	v_cndmask_b32_e64 v29, v29, v25, s[60:61]
	v_pk_fma_f16 v6, v2, v130, v131 op_sel:[0,1,1] op_sel_hi:[1,1,1] neg_lo:[1,0,0] neg_hi:[1,0,0]
	v_pk_fma_f16 v7, v3, v130, v131 op_sel:[0,1,1] op_sel_hi:[1,1,1] neg_lo:[1,0,0] neg_hi:[1,0,0]
	v_pk_fma_f16 v8, v4, v130, v131 op_sel:[0,1,1] op_sel_hi:[1,1,1] neg_lo:[1,0,0] neg_hi:[1,0,0]
	v_pk_fma_f16 v9, v5, v130, v131 op_sel:[0,1,1] op_sel_hi:[1,1,1] neg_lo:[1,0,0] neg_hi:[1,0,0]
	v_mfma_f32_16x16x32_f16 v[22:25], v[10:13], v[2:5], 0
	ds_read2_b64 v[84:87], v32 offset0:9 offset1:211
	v_pk_fma_f16 v2, v68, v6, v2
	v_pk_fma_f16 v3, v69, v7, v3
	v_pk_fma_f16 v4, v70, v8, v4
	v_pk_fma_f16 v5, v71, v9, v5
	v_cndmask_b32_e64 v26, v26, v18, s[62:63]
	s_waitcnt lgkmcnt(3)
	v_pk_fma_f16 v6, v2, v132, v133 op_sel:[0,1,1] op_sel_hi:[1,1,1] neg_lo:[1,0,0] neg_hi:[1,0,0]
	v_pk_fma_f16 v7, v3, v132, v133 op_sel:[0,1,1] op_sel_hi:[1,1,1] neg_lo:[1,0,0] neg_hi:[1,0,0]
	v_pk_fma_f16 v8, v4, v132, v133 op_sel:[0,1,1] op_sel_hi:[1,1,1] neg_lo:[1,0,0] neg_hi:[1,0,0]
	v_pk_fma_f16 v9, v5, v132, v133 op_sel:[0,1,1] op_sel_hi:[1,1,1] neg_lo:[1,0,0] neg_hi:[1,0,0]
	v_mfma_f32_16x16x32_f16 v[18:21], v[10:13], v[2:5], 0
	ds_read2_b64 v[88:91], v32 offset0:10 offset1:212
	ds_read_b128 v[140:143], v33 offset:80
	v_pk_fma_f16 v2, v72, v6, v2
	v_pk_fma_f16 v3, v73, v7, v3
	v_pk_fma_f16 v4, v74, v8, v4
	v_pk_fma_f16 v5, v75, v9, v5
	v_cndmask_b32_e64 v27, v27, v23, s[62:63]
	v_pk_fma_f16 v6, v2, v134, v135 op_sel:[0,1,1] op_sel_hi:[1,1,1] neg_lo:[1,0,0] neg_hi:[1,0,0]
	v_pk_fma_f16 v7, v3, v134, v135 op_sel:[0,1,1] op_sel_hi:[1,1,1] neg_lo:[1,0,0] neg_hi:[1,0,0]
	v_pk_fma_f16 v8, v4, v134, v135 op_sel:[0,1,1] op_sel_hi:[1,1,1] neg_lo:[1,0,0] neg_hi:[1,0,0]
	v_pk_fma_f16 v9, v5, v134, v135 op_sel:[0,1,1] op_sel_hi:[1,1,1] neg_lo:[1,0,0] neg_hi:[1,0,0]
	v_mfma_f32_16x16x32_f16 v[22:25], v[10:13], v[2:5], 0
	ds_read2_b64 v[92:95], v32 offset0:11 offset1:213
	v_pk_fma_f16 v2, v76, v6, v2
	v_pk_fma_f16 v3, v77, v7, v3
	v_pk_fma_f16 v4, v78, v8, v4
	v_pk_fma_f16 v5, v79, v9, v5
	v_cndmask_b32_e64 v28, v28, v20, s[62:63]
	s_waitcnt lgkmcnt(3)
	v_pk_fma_f16 v6, v2, v136, v137 op_sel:[0,1,1] op_sel_hi:[1,1,1] neg_lo:[1,0,0] neg_hi:[1,0,0]
	v_pk_fma_f16 v7, v3, v136, v137 op_sel:[0,1,1] op_sel_hi:[1,1,1] neg_lo:[1,0,0] neg_hi:[1,0,0]
	v_pk_fma_f16 v8, v4, v136, v137 op_sel:[0,1,1] op_sel_hi:[1,1,1] neg_lo:[1,0,0] neg_hi:[1,0,0]
	v_pk_fma_f16 v9, v5, v136, v137 op_sel:[0,1,1] op_sel_hi:[1,1,1] neg_lo:[1,0,0] neg_hi:[1,0,0]
	v_mfma_f32_16x16x32_f16 v[18:21], v[10:13], v[2:5], 0
	ds_read2_b64 v[96:99], v32 offset0:12 offset1:214
	ds_read_b128 v[144:147], v33 offset:96
	v_pk_fma_f16 v2, v80, v6, v2
	v_pk_fma_f16 v3, v81, v7, v3
	v_pk_fma_f16 v4, v82, v8, v4
	v_pk_fma_f16 v5, v83, v9, v5
	v_cndmask_b32_e64 v29, v29, v25, s[62:63]
	v_readfirstlane_b32 s4, v37
	v_readfirstlane_b32 s5, v38
	s_and_b32 s4, s4, s5
	s_cbranch_scc0 .Lc1_slow0

.Lc1_nd0:
	v_pk_fma_f16 v6, v2, v138, v139 op_sel:[0,1,1] op_sel_hi:[1,1,1] neg_lo:[1,0,0] neg_hi:[1,0,0]
	v_pk_fma_f16 v7, v3, v138, v139 op_sel:[0,1,1] op_sel_hi:[1,1,1] neg_lo:[1,0,0] neg_hi:[1,0,0]
	v_pk_fma_f16 v8, v4, v138, v139 op_sel:[0,1,1] op_sel_hi:[1,1,1] neg_lo:[1,0,0] neg_hi:[1,0,0]
	v_pk_fma_f16 v9, v5, v138, v139 op_sel:[0,1,1] op_sel_hi:[1,1,1] neg_lo:[1,0,0] neg_hi:[1,0,0]
	v_mfma_f32_16x16x32_f16 v[22:25], v[10:13], v[2:5], 0
	ds_read2_b64 v[100:103], v32 offset0:13 offset1:215
	v_pk_fma_f16 v2, v84, v6, v2
	v_pk_fma_f16 v3, v85, v7, v3
	v_pk_fma_f16 v4, v86, v8, v4
	v_pk_fma_f16 v5, v87, v9, v5
	v_cndmask_b32_e64 v26, v26, v18, s[64:65]
	s_waitcnt lgkmcnt(3)
	v_pk_fma_f16 v6, v2, v140, v141 op_sel:[0,1,1] op_sel_hi:[1,1,1] neg_lo:[1,0,0] neg_hi:[1,0,0]
	v_pk_fma_f16 v7, v3, v140, v141 op_sel:[0,1,1] op_sel_hi:[1,1,1] neg_lo:[1,0,0] neg_hi:[1,0,0]
	v_pk_fma_f16 v8, v4, v140, v141 op_sel:[0,1,1] op_sel_hi:[1,1,1] neg_lo:[1,0,0] neg_hi:[1,0,0]
	v_pk_fma_f16 v9, v5, v140, v141 op_sel:[0,1,1] op_sel_hi:[1,1,1] neg_lo:[1,0,0] neg_hi:[1,0,0]
	v_mfma_f32_16x16x32_f16 v[18:21], v[10:13], v[2:5], 0
	ds_read2_b64 v[104:107], v32 offset0:14 offset1:216
	ds_read_b128 v[148:151], v33 offset:112
	v_pk_fma_f16 v2, v88, v6, v2
	v_pk_fma_f16 v3, v89, v7, v3
	v_pk_fma_f16 v4, v90, v8, v4
	v_pk_fma_f16 v5, v91, v9, v5
	v_cndmask_b32_e64 v27, v27, v23, s[64:65]
	v_pk_fma_f16 v6, v2, v142, v143 op_sel:[0,1,1] op_sel_hi:[1,1,1] neg_lo:[1,0,0] neg_hi:[1,0,0]
	v_pk_fma_f16 v7, v3, v142, v143 op_sel:[0,1,1] op_sel_hi:[1,1,1] neg_lo:[1,0,0] neg_hi:[1,0,0]
	v_pk_fma_f16 v8, v4, v142, v143 op_sel:[0,1,1] op_sel_hi:[1,1,1] neg_lo:[1,0,0] neg_hi:[1,0,0]
	v_pk_fma_f16 v9, v5, v142, v143 op_sel:[0,1,1] op_sel_hi:[1,1,1] neg_lo:[1,0,0] neg_hi:[1,0,0]
	v_mfma_f32_16x16x32_f16 v[22:25], v[10:13], v[2:5], 0
	ds_read2_b64 v[108:111], v32 offset0:15 offset1:217
	v_pk_fma_f16 v2, v92, v6, v2
	v_pk_fma_f16 v3, v93, v7, v3
	v_pk_fma_f16 v4, v94, v8, v4
	v_pk_fma_f16 v5, v95, v9, v5
	v_cndmask_b32_e64 v28, v28, v20, s[64:65]
	s_waitcnt lgkmcnt(3)
	v_pk_fma_f16 v6, v2, v144, v145 op_sel:[0,1,1] op_sel_hi:[1,1,1] neg_lo:[1,0,0] neg_hi:[1,0,0]
	v_pk_fma_f16 v7, v3, v144, v145 op_sel:[0,1,1] op_sel_hi:[1,1,1] neg_lo:[1,0,0] neg_hi:[1,0,0]
	v_pk_fma_f16 v8, v4, v144, v145 op_sel:[0,1,1] op_sel_hi:[1,1,1] neg_lo:[1,0,0] neg_hi:[1,0,0]
	v_pk_fma_f16 v9, v5, v144, v145 op_sel:[0,1,1] op_sel_hi:[1,1,1] neg_lo:[1,0,0] neg_hi:[1,0,0]
	v_mfma_f32_16x16x32_f16 v[18:21], v[10:13], v[2:5], 0
	ds_read2_b64 v[48:51], v32 offset0:16 offset1:218
	ds_read_b128 v[120:123], v33 offset:128
	ds_read2_b64 v[14:17], v34 offset0:16 offset1:218
	v_pk_fma_f16 v2, v96, v6, v2
	v_pk_fma_f16 v3, v97, v7, v3
	v_pk_fma_f16 v4, v98, v8, v4
	v_pk_fma_f16 v5, v99, v9, v5
	v_cndmask_b32_e64 v29, v29, v25, s[64:65]
	s_cmp_eq_u32 s72, 1
	s_cbranch_scc0 .Lc1_ns0
	s_waitcnt lgkmcnt(7)
	v_readfirstlane_b32 s4, v45
	s_cmp_eq_u32 s4, 4
	s_cbranch_scc0 .Lc1_dslow0

.Lc1_ns0:
	v_pk_fma_f16 v6, v2, v146, v147 op_sel:[0,1,1] op_sel_hi:[1,1,1] neg_lo:[1,0,0] neg_hi:[1,0,0]
	v_pk_fma_f16 v7, v3, v146, v147 op_sel:[0,1,1] op_sel_hi:[1,1,1] neg_lo:[1,0,0] neg_hi:[1,0,0]
	v_pk_fma_f16 v8, v4, v146, v147 op_sel:[0,1,1] op_sel_hi:[1,1,1] neg_lo:[1,0,0] neg_hi:[1,0,0]
	v_pk_fma_f16 v9, v5, v146, v147 op_sel:[0,1,1] op_sel_hi:[1,1,1] neg_lo:[1,0,0] neg_hi:[1,0,0]
	v_mfma_f32_16x16x32_f16 v[22:25], v[10:13], v[2:5], 0
	ds_read2_b64 v[52:55], v32 offset0:17 offset1:219
	v_pk_fma_f16 v2, v100, v6, v2
	v_pk_fma_f16 v3, v101, v7, v3
	v_pk_fma_f16 v4, v102, v8, v4
	v_pk_fma_f16 v5, v103, v9, v5
	v_cndmask_b32_e64 v26, v26, v18, s[66:67]
	s_waitcnt lgkmcnt(4)
	v_pk_fma_f16 v6, v2, v148, v149 op_sel:[0,1,1] op_sel_hi:[1,1,1] neg_lo:[1,0,0] neg_hi:[1,0,0]
	v_pk_fma_f16 v7, v3, v148, v149 op_sel:[0,1,1] op_sel_hi:[1,1,1] neg_lo:[1,0,0] neg_hi:[1,0,0]
	v_pk_fma_f16 v8, v4, v148, v149 op_sel:[0,1,1] op_sel_hi:[1,1,1] neg_lo:[1,0,0] neg_hi:[1,0,0]
	v_pk_fma_f16 v9, v5, v148, v149 op_sel:[0,1,1] op_sel_hi:[1,1,1] neg_lo:[1,0,0] neg_hi:[1,0,0]
	v_mfma_f32_16x16x32_f16 v[18:21], v[10:13], v[2:5], 0
	ds_read2_b64 v[56:59], v32 offset0:18 offset1:220
	ds_read_b128 v[124:127], v33 offset:144
	v_pk_fma_f16 v2, v104, v6, v2
	v_pk_fma_f16 v3, v105, v7, v3
	v_pk_fma_f16 v4, v106, v8, v4
	v_pk_fma_f16 v5, v107, v9, v5
	v_cndmask_b32_e64 v27, v27, v23, s[66:67]
	v_pk_fma_f16 v6, v2, v150, v151 op_sel:[0,1,1] op_sel_hi:[1,1,1] neg_lo:[1,0,0] neg_hi:[1,0,0]
	v_pk_fma_f16 v7, v3, v150, v151 op_sel:[0,1,1] op_sel_hi:[1,1,1] neg_lo:[1,0,0] neg_hi:[1,0,0]
	v_pk_fma_f16 v8, v4, v150, v151 op_sel:[0,1,1] op_sel_hi:[1,1,1] neg_lo:[1,0,0] neg_hi:[1,0,0]
	v_pk_fma_f16 v9, v5, v150, v151 op_sel:[0,1,1] op_sel_hi:[1,1,1] neg_lo:[1,0,0] neg_hi:[1,0,0]
	v_mfma_f32_16x16x32_f16 v[22:25], v[10:13], v[2:5], 0
	ds_read2_b64 v[60:63], v32 offset0:19 offset1:221
	v_pk_fma_f16 v2, v108, v6, v2
	v_pk_fma_f16 v3, v109, v7, v3
	v_pk_fma_f16 v4, v110, v8, v4
	v_pk_fma_f16 v5, v111, v9, v5
	v_cndmask_b32_e64 v28, v28, v20, s[66:67]
.Lc1_next0:
	s_waitcnt lgkmcnt(3)
	v_pk_fma_f16 v6, v2, v120, v121 op_sel:[0,1,1] op_sel_hi:[1,1,1] neg_lo:[1,0,0] neg_hi:[1,0,0]
	v_pk_fma_f16 v7, v3, v120, v121 op_sel:[0,1,1] op_sel_hi:[1,1,1] neg_lo:[1,0,0] neg_hi:[1,0,0]
	v_pk_fma_f16 v8, v4, v120, v121 op_sel:[0,1,1] op_sel_hi:[1,1,1] neg_lo:[1,0,0] neg_hi:[1,0,0]
	v_pk_fma_f16 v9, v5, v120, v121 op_sel:[0,1,1] op_sel_hi:[1,1,1] neg_lo:[1,0,0] neg_hi:[1,0,0]
	v_mfma_f32_16x16x32_f16 v[18:21], v[14:17], v[2:5], 0
	ds_read2_b64 v[64:67], v32 offset0:20 offset1:222
	ds_read_b128 v[128:131], v33 offset:160
	ds_read_b32 v37, v36 offset:8
	ds_read_b32 v38, v36 offset:72
	v_pk_fma_f16 v2, v48, v6, v2
	v_pk_fma_f16 v3, v49, v7, v3
	v_pk_fma_f16 v4, v50, v8, v4
	v_pk_fma_f16 v5, v51, v9, v5
	v_cndmask_b32_e64 v29, v29, v25, s[66:67]
	v_cvt_pk_f16_f32 v30, v26, v27
	v_cvt_pk_f16_f32 v31, v28, v29
	ds_write_b16 v39, v30 offset:2048
	ds_write_b16_d16_hi v39, v30 offset:2112
	ds_write_b16 v39, v31 offset:2176
	ds_write_b16_d16_hi v39, v31 offset:2240
	s_mov_b64 exec, 1
	ds_add_u32 v36, v44 offset:128
	s_mov_b64 exec, -1
	v_pk_fma_f16 v6, v2, v122, v123 op_sel:[0,1,1] op_sel_hi:[1,1,1] neg_lo:[1,0,0] neg_hi:[1,0,0]
	v_pk_fma_f16 v7, v3, v122, v123 op_sel:[0,1,1] op_sel_hi:[1,1,1] neg_lo:[1,0,0] neg_hi:[1,0,0]
	v_pk_fma_f16 v8, v4, v122, v123 op_sel:[0,1,1] op_sel_hi:[1,1,1] neg_lo:[1,0,0] neg_hi:[1,0,0]
	v_pk_fma_f16 v9, v5, v122, v123 op_sel:[0,1,1] op_sel_hi:[1,1,1] neg_lo:[1,0,0] neg_hi:[1,0,0]
	v_mfma_f32_16x16x32_f16 v[22:25], v[14:17], v[2:5], 0
	ds_read2_b64 v[68:71], v32 offset0:21 offset1:223
	v_pk_fma_f16 v2, v52, v6, v2
	v_pk_fma_f16 v3, v53, v7, v3
	v_pk_fma_f16 v4, v54, v8, v4
	v_pk_fma_f16 v5, v55, v9, v5
	v_cndmask_b32_e64 v26, v26, v18, s[60:61]
	s_waitcnt lgkmcnt(10)
	v_pk_fma_f16 v6, v2, v124, v125 op_sel:[0,1,1] op_sel_hi:[1,1,1] neg_lo:[1,0,0] neg_hi:[1,0,0]
	v_pk_fma_f16 v7, v3, v124, v125 op_sel:[0,1,1] op_sel_hi:[1,1,1] neg_lo:[1,0,0] neg_hi:[1,0,0]
	v_pk_fma_f16 v8, v4, v124, v125 op_sel:[0,1,1] op_sel_hi:[1,1,1] neg_lo:[1,0,0] neg_hi:[1,0,0]
	v_pk_fma_f16 v9, v5, v124, v125 op_sel:[0,1,1] op_sel_hi:[1,1,1] neg_lo:[1,0,0] neg_hi:[1,0,0]
	v_mfma_f32_16x16x32_f16 v[18:21], v[14:17], v[2:5], 0
	ds_read2_b64 v[72:75], v32 offset0:22 offset1:224
	ds_read_b128 v[132:135], v33 offset:176
	v_pk_fma_f16 v2, v56, v6, v2
	v_pk_fma_f16 v3, v57, v7, v3
	v_pk_fma_f16 v4, v58, v8, v4
	v_pk_fma_f16 v5, v59, v9, v5
	v_cndmask_b32_e64 v27, v27, v23, s[60:61]
	v_pk_fma_f16 v6, v2, v126, v127 op_sel:[0,1,1] op_sel_hi:[1,1,1] neg_lo:[1,0,0] neg_hi:[1,0,0]
	v_pk_fma_f16 v7, v3, v126, v127 op_sel:[0,1,1] op_sel_hi:[1,1,1] neg_lo:[1,0,0] neg_hi:[1,0,0]
	v_pk_fma_f16 v8, v4, v126, v127 op_sel:[0,1,1] op_sel_hi:[1,1,1] neg_lo:[1,0,0] neg_hi:[1,0,0]
	v_pk_fma_f16 v9, v5, v126, v127 op_sel:[0,1,1] op_sel_hi:[1,1,1] neg_lo:[1,0,0] neg_hi:[1,0,0]
	v_mfma_f32_16x16x32_f16 v[22:25], v[14:17], v[2:5], 0
	ds_read2_b64 v[76:79], v32 offset0:23 offset1:225
	v_pk_fma_f16 v2, v60, v6, v2
	v_pk_fma_f16 v3, v61, v7, v3
	v_pk_fma_f16 v4, v62, v8, v4
	v_pk_fma_f16 v5, v63, v9, v5
	v_cndmask_b32_e64 v28, v28, v20, s[60:61]
	s_waitcnt lgkmcnt(3)
	v_pk_fma_f16 v6, v2, v128, v129 op_sel:[0,1,1] op_sel_hi:[1,1,1] neg_lo:[1,0,0] neg_hi:[1,0,0]
	v_pk_fma_f16 v7, v3, v128, v129 op_sel:[0,1,1] op_sel_hi:[1,1,1] neg_lo:[1,0,0] neg_hi:[1,0,0]
	v_pk_fma_f16 v8, v4, v128, v129 op_sel:[0,1,1] op_sel_hi:[1,1,1] neg_lo:[1,0,0] neg_hi:[1,0,0]
	v_pk_fma_f16 v9, v5, v128, v129 op_sel:[0,1,1] op_sel_hi:[1,1,1] neg_lo:[1,0,0] neg_hi:[1,0,0]
	v_mfma_f32_16x16x32_f16 v[18:21], v[14:17], v[2:5], 0
	ds_read2_b64 v[80:83], v32 offset0:24 offset1:226
	ds_read_b128 v[136:139], v33 offset:192
	v_pk_fma_f16 v2, v64, v6, v2
	v_pk_fma_f16 v3, v65, v7, v3
	v_pk_fma_f16 v4, v66, v8, v4
	v_pk_fma_f16 v5, v67, v9, v5
	v_cndmask_b32_e64 v29, v29, v25, s[60:61]
	v_pk_fma_f16 v6, v2, v130, v131 op_sel:[0,1,1] op_sel_hi:[1,1,1] neg_lo:[1,0,0] neg_hi:[1,0,0]
	v_pk_fma_f16 v7, v3, v130, v131 op_sel:[0,1,1] op_sel_hi:[1,1,1] neg_lo:[1,0,0] neg_hi:[1,0,0]
	v_pk_fma_f16 v8, v4, v130, v131 op_sel:[0,1,1] op_sel_hi:[1,1,1] neg_lo:[1,0,0] neg_hi:[1,0,0]
	v_pk_fma_f16 v9, v5, v130, v131 op_sel:[0,1,1] op_sel_hi:[1,1,1] neg_lo:[1,0,0] neg_hi:[1,0,0]
	v_mfma_f32_16x16x32_f16 v[22:25], v[14:17], v[2:5], 0
	ds_read2_b64 v[84:87], v32 offset0:25 offset1:227
	v_pk_fma_f16 v2, v68, v6, v2
	v_pk_fma_f16 v3, v69, v7, v3
	v_pk_fma_f16 v4, v70, v8, v4
	v_pk_fma_f16 v5, v71, v9, v5
	v_cndmask_b32_e64 v26, v26, v18, s[62:63]
	s_waitcnt lgkmcnt(3)
	v_pk_fma_f16 v6, v2, v132, v133 op_sel:[0,1,1] op_sel_hi:[1,1,1] neg_lo:[1,0,0] neg_hi:[1,0,0]
	v_pk_fma_f16 v7, v3, v132, v133 op_sel:[0,1,1] op_sel_hi:[1,1,1] neg_lo:[1,0,0] neg_hi:[1,0,0]
	v_pk_fma_f16 v8, v4, v132, v133 op_sel:[0,1,1] op_sel_hi:[1,1,1] neg_lo:[1,0,0] neg_hi:[1,0,0]
	v_pk_fma_f16 v9, v5, v132, v133 op_sel:[0,1,1] op_sel_hi:[1,1,1] neg_lo:[1,0,0] neg_hi:[1,0,0]
	v_mfma_f32_16x16x32_f16 v[18:21], v[14:17], v[2:5], 0
	ds_read2_b64 v[88:91], v32 offset0:26 offset1:228
	ds_read_b128 v[140:143], v33 offset:208
	v_pk_fma_f16 v2, v72, v6, v2
	v_pk_fma_f16 v3, v73, v7, v3
	v_pk_fma_f16 v4, v74, v8, v4
	v_pk_fma_f16 v5, v75, v9, v5
	v_cndmask_b32_e64 v27, v27, v23, s[62:63]
	v_pk_fma_f16 v6, v2, v134, v135 op_sel:[0,1,1] op_sel_hi:[1,1,1] neg_lo:[1,0,0] neg_hi:[1,0,0]
	v_pk_fma_f16 v7, v3, v134, v135 op_sel:[0,1,1] op_sel_hi:[1,1,1] neg_lo:[1,0,0] neg_hi:[1,0,0]
	v_pk_fma_f16 v8, v4, v134, v135 op_sel:[0,1,1] op_sel_hi:[1,1,1] neg_lo:[1,0,0] neg_hi:[1,0,0]
	v_pk_fma_f16 v9, v5, v134, v135 op_sel:[0,1,1] op_sel_hi:[1,1,1] neg_lo:[1,0,0] neg_hi:[1,0,0]
	v_mfma_f32_16x16x32_f16 v[22:25], v[14:17], v[2:5], 0
	ds_read2_b64 v[92:95], v32 offset0:27 offset1:229
	v_pk_fma_f16 v2, v76, v6, v2
	v_pk_fma_f16 v3, v77, v7, v3
	v_pk_fma_f16 v4, v78, v8, v4
	v_pk_fma_f16 v5, v79, v9, v5
	v_cndmask_b32_e64 v28, v28, v20, s[62:63]
	s_waitcnt lgkmcnt(3)
	v_pk_fma_f16 v6, v2, v136, v137 op_sel:[0,1,1] op_sel_hi:[1,1,1] neg_lo:[1,0,0] neg_hi:[1,0,0]
	v_pk_fma_f16 v7, v3, v136, v137 op_sel:[0,1,1] op_sel_hi:[1,1,1] neg_lo:[1,0,0] neg_hi:[1,0,0]
	v_pk_fma_f16 v8, v4, v136, v137 op_sel:[0,1,1] op_sel_hi:[1,1,1] neg_lo:[1,0,0] neg_hi:[1,0,0]
	v_pk_fma_f16 v9, v5, v136, v137 op_sel:[0,1,1] op_sel_hi:[1,1,1] neg_lo:[1,0,0] neg_hi:[1,0,0]
	v_mfma_f32_16x16x32_f16 v[18:21], v[14:17], v[2:5], 0
	ds_read2_b64 v[96:99], v32 offset0:28 offset1:230
	ds_read_b128 v[144:147], v33 offset:224
	v_pk_fma_f16 v2, v80, v6, v2
	v_pk_fma_f16 v3, v81, v7, v3
	v_pk_fma_f16 v4, v82, v8, v4
	v_pk_fma_f16 v5, v83, v9, v5
	v_cndmask_b32_e64 v29, v29, v25, s[62:63]
	v_readfirstlane_b32 s4, v37
	v_readfirstlane_b32 s5, v38
	s_and_b32 s4, s4, s5
	s_cbranch_scc0 .Lc1_slow1

.Lc1_nd1:
	v_pk_fma_f16 v6, v2, v138, v139 op_sel:[0,1,1] op_sel_hi:[1,1,1] neg_lo:[1,0,0] neg_hi:[1,0,0]
	v_pk_fma_f16 v7, v3, v138, v139 op_sel:[0,1,1] op_sel_hi:[1,1,1] neg_lo:[1,0,0] neg_hi:[1,0,0]
	v_pk_fma_f16 v8, v4, v138, v139 op_sel:[0,1,1] op_sel_hi:[1,1,1] neg_lo:[1,0,0] neg_hi:[1,0,0]
	v_pk_fma_f16 v9, v5, v138, v139 op_sel:[0,1,1] op_sel_hi:[1,1,1] neg_lo:[1,0,0] neg_hi:[1,0,0]
	v_mfma_f32_16x16x32_f16 v[22:25], v[14:17], v[2:5], 0
	ds_read2_b64 v[100:103], v32 offset0:29 offset1:231
	v_pk_fma_f16 v2, v84, v6, v2
	v_pk_fma_f16 v3, v85, v7, v3
	v_pk_fma_f16 v4, v86, v8, v4
	v_pk_fma_f16 v5, v87, v9, v5
	v_cndmask_b32_e64 v26, v26, v18, s[64:65]
	s_waitcnt lgkmcnt(3)
	v_pk_fma_f16 v6, v2, v140, v141 op_sel:[0,1,1] op_sel_hi:[1,1,1] neg_lo:[1,0,0] neg_hi:[1,0,0]
	v_pk_fma_f16 v7, v3, v140, v141 op_sel:[0,1,1] op_sel_hi:[1,1,1] neg_lo:[1,0,0] neg_hi:[1,0,0]
	v_pk_fma_f16 v8, v4, v140, v141 op_sel:[0,1,1] op_sel_hi:[1,1,1] neg_lo:[1,0,0] neg_hi:[1,0,0]
	v_pk_fma_f16 v9, v5, v140, v141 op_sel:[0,1,1] op_sel_hi:[1,1,1] neg_lo:[1,0,0] neg_hi:[1,0,0]
	v_mfma_f32_16x16x32_f16 v[18:21], v[14:17], v[2:5], 0
	ds_read2_b64 v[104:107], v32 offset0:30 offset1:232
	ds_read_b128 v[148:151], v33 offset:240
	v_pk_fma_f16 v2, v88, v6, v2
	v_pk_fma_f16 v3, v89, v7, v3
	v_pk_fma_f16 v4, v90, v8, v4
	v_pk_fma_f16 v5, v91, v9, v5
	v_cndmask_b32_e64 v27, v27, v23, s[64:65]
	v_pk_fma_f16 v6, v2, v142, v143 op_sel:[0,1,1] op_sel_hi:[1,1,1] neg_lo:[1,0,0] neg_hi:[1,0,0]
	v_pk_fma_f16 v7, v3, v142, v143 op_sel:[0,1,1] op_sel_hi:[1,1,1] neg_lo:[1,0,0] neg_hi:[1,0,0]
	v_pk_fma_f16 v8, v4, v142, v143 op_sel:[0,1,1] op_sel_hi:[1,1,1] neg_lo:[1,0,0] neg_hi:[1,0,0]
	v_pk_fma_f16 v9, v5, v142, v143 op_sel:[0,1,1] op_sel_hi:[1,1,1] neg_lo:[1,0,0] neg_hi:[1,0,0]
	v_mfma_f32_16x16x32_f16 v[22:25], v[14:17], v[2:5], 0
	ds_read2_b64 v[108:111], v32 offset0:31 offset1:233
	v_pk_fma_f16 v2, v92, v6, v2
	v_pk_fma_f16 v3, v93, v7, v3
	v_pk_fma_f16 v4, v94, v8, v4
	v_pk_fma_f16 v5, v95, v9, v5
	v_cndmask_b32_e64 v28, v28, v20, s[64:65]
	s_waitcnt lgkmcnt(3)
	v_pk_fma_f16 v6, v2, v144, v145 op_sel:[0,1,1] op_sel_hi:[1,1,1] neg_lo:[1,0,0] neg_hi:[1,0,0]
	v_pk_fma_f16 v7, v3, v144, v145 op_sel:[0,1,1] op_sel_hi:[1,1,1] neg_lo:[1,0,0] neg_hi:[1,0,0]
	v_pk_fma_f16 v8, v4, v144, v145 op_sel:[0,1,1] op_sel_hi:[1,1,1] neg_lo:[1,0,0] neg_hi:[1,0,0]
	v_pk_fma_f16 v9, v5, v144, v145 op_sel:[0,1,1] op_sel_hi:[1,1,1] neg_lo:[1,0,0] neg_hi:[1,0,0]
	v_mfma_f32_16x16x32_f16 v[18:21], v[14:17], v[2:5], 0
	ds_read2_b64 v[48:51], v32 offset0:32 offset1:234
	ds_read_b128 v[120:123], v33 offset:256
	ds_read2_b64 v[10:13], v34 offset0:32 offset1:234
	v_pk_fma_f16 v2, v96, v6, v2
	v_pk_fma_f16 v3, v97, v7, v3
	v_pk_fma_f16 v4, v98, v8, v4
	v_pk_fma_f16 v5, v99, v9, v5
	v_cndmask_b32_e64 v29, v29, v25, s[64:65]
	s_cmp_eq_u32 s72, 1
	s_cbranch_scc0 .Lc1_ns1
	s_waitcnt lgkmcnt(7)
	v_readfirstlane_b32 s4, v45
	s_cmp_eq_u32 s4, 4
	s_cbranch_scc0 .Lc1_dslow1

.Lc1_ns1:
	v_pk_fma_f16 v6, v2, v146, v147 op_sel:[0,1,1] op_sel_hi:[1,1,1] neg_lo:[1,0,0] neg_hi:[1,0,0]
	v_pk_fma_f16 v7, v3, v146, v147 op_sel:[0,1,1] op_sel_hi:[1,1,1] neg_lo:[1,0,0] neg_hi:[1,0,0]
	v_pk_fma_f16 v8, v4, v146, v147 op_sel:[0,1,1] op_sel_hi:[1,1,1] neg_lo:[1,0,0] neg_hi:[1,0,0]
	v_pk_fma_f16 v9, v5, v146, v147 op_sel:[0,1,1] op_sel_hi:[1,1,1] neg_lo:[1,0,0] neg_hi:[1,0,0]
	v_mfma_f32_16x16x32_f16 v[22:25], v[14:17], v[2:5], 0
	ds_read2_b64 v[52:55], v32 offset0:33 offset1:235
	v_pk_fma_f16 v2, v100, v6, v2
	v_pk_fma_f16 v3, v101, v7, v3
	v_pk_fma_f16 v4, v102, v8, v4
	v_pk_fma_f16 v5, v103, v9, v5
	v_cndmask_b32_e64 v26, v26, v18, s[66:67]
	s_waitcnt lgkmcnt(4)
	v_pk_fma_f16 v6, v2, v148, v149 op_sel:[0,1,1] op_sel_hi:[1,1,1] neg_lo:[1,0,0] neg_hi:[1,0,0]
	v_pk_fma_f16 v7, v3, v148, v149 op_sel:[0,1,1] op_sel_hi:[1,1,1] neg_lo:[1,0,0] neg_hi:[1,0,0]
	v_pk_fma_f16 v8, v4, v148, v149 op_sel:[0,1,1] op_sel_hi:[1,1,1] neg_lo:[1,0,0] neg_hi:[1,0,0]
	v_pk_fma_f16 v9, v5, v148, v149 op_sel:[0,1,1] op_sel_hi:[1,1,1] neg_lo:[1,0,0] neg_hi:[1,0,0]
	v_mfma_f32_16x16x32_f16 v[18:21], v[14:17], v[2:5], 0
	ds_read2_b64 v[56:59], v32 offset0:34 offset1:236
	ds_read_b128 v[124:127], v33 offset:272
	v_pk_fma_f16 v2, v104, v6, v2
	v_pk_fma_f16 v3, v105, v7, v3
	v_pk_fma_f16 v4, v106, v8, v4
	v_pk_fma_f16 v5, v107, v9, v5
	v_cndmask_b32_e64 v27, v27, v23, s[66:67]
	v_pk_fma_f16 v6, v2, v150, v151 op_sel:[0,1,1] op_sel_hi:[1,1,1] neg_lo:[1,0,0] neg_hi:[1,0,0]
	v_pk_fma_f16 v7, v3, v150, v151 op_sel:[0,1,1] op_sel_hi:[1,1,1] neg_lo:[1,0,0] neg_hi:[1,0,0]
	v_pk_fma_f16 v8, v4, v150, v151 op_sel:[0,1,1] op_sel_hi:[1,1,1] neg_lo:[1,0,0] neg_hi:[1,0,0]
	v_pk_fma_f16 v9, v5, v150, v151 op_sel:[0,1,1] op_sel_hi:[1,1,1] neg_lo:[1,0,0] neg_hi:[1,0,0]
	v_mfma_f32_16x16x32_f16 v[22:25], v[14:17], v[2:5], 0
	ds_read2_b64 v[60:63], v32 offset0:35 offset1:237
	v_pk_fma_f16 v2, v108, v6, v2
	v_pk_fma_f16 v3, v109, v7, v3
	v_pk_fma_f16 v4, v110, v8, v4
	v_pk_fma_f16 v5, v111, v9, v5
	v_cndmask_b32_e64 v28, v28, v20, s[66:67]
.Lc1_next1:
	v_add_u32_e32 v32, 0x100, v32
	v_add_u32_e32 v33, 0x100, v33
	v_add_u32_e32 v34, 0x100, v34
	v_add_u32_e32 v36, 8, v36
	v_add_u32_e32 v39, 0x1000, v39
	v_add_u32_e32 v43, 0x1000, v43
	v_add_u32_e32 v35, 0x800, v35
	s_xor_b32 s71, s71, 2
	s_add_i32 s70, s70, 1
	s_cmp_lt_u32 s70, 6
	s_cbranch_scc1 .Lc1_loop
	s_waitcnt lgkmcnt(3)
	v_pk_fma_f16 v6, v2, v120, v121 op_sel:[0,1,1] op_sel_hi:[1,1,1] neg_lo:[1,0,0] neg_hi:[1,0,0]
	v_pk_fma_f16 v7, v3, v120, v121 op_sel:[0,1,1] op_sel_hi:[1,1,1] neg_lo:[1,0,0] neg_hi:[1,0,0]
	v_pk_fma_f16 v8, v4, v120, v121 op_sel:[0,1,1] op_sel_hi:[1,1,1] neg_lo:[1,0,0] neg_hi:[1,0,0]
	v_pk_fma_f16 v9, v5, v120, v121 op_sel:[0,1,1] op_sel_hi:[1,1,1] neg_lo:[1,0,0] neg_hi:[1,0,0]
	v_mfma_f32_16x16x32_f16 v[18:21], v[10:13], v[2:5], 0
	ds_read2_b64 v[64:67], v32 offset0:4 offset1:206
	ds_read_b128 v[128:131], v33 offset:32
	v_pk_fma_f16 v2, v48, v6, v2
	v_pk_fma_f16 v3, v49, v7, v3
	v_pk_fma_f16 v4, v50, v8, v4
	v_pk_fma_f16 v5, v51, v9, v5
	v_cndmask_b32_e64 v29, v29, v25, s[66:67]
	v_cvt_pk_f16_f32 v30, v26, v27
	v_cvt_pk_f16_f32 v31, v28, v29
	ds_write_b16 v39, v30 offset:0
	ds_write_b16_d16_hi v39, v30 offset:64
	ds_write_b16 v39, v31 offset:128
	ds_write_b16_d16_hi v39, v31 offset:192
	s_mov_b64 exec, 1
	ds_add_u32 v36, v44 offset:124
	s_mov_b64 exec, -1
	v_pk_fma_f16 v6, v2, v122, v123 op_sel:[0,1,1] op_sel_hi:[1,1,1] neg_lo:[1,0,0] neg_hi:[1,0,0]
	v_pk_fma_f16 v7, v3, v122, v123 op_sel:[0,1,1] op_sel_hi:[1,1,1] neg_lo:[1,0,0] neg_hi:[1,0,0]
	v_pk_fma_f16 v8, v4, v122, v123 op_sel:[0,1,1] op_sel_hi:[1,1,1] neg_lo:[1,0,0] neg_hi:[1,0,0]
	v_pk_fma_f16 v9, v5, v122, v123 op_sel:[0,1,1] op_sel_hi:[1,1,1] neg_lo:[1,0,0] neg_hi:[1,0,0]
	v_mfma_f32_16x16x32_f16 v[22:25], v[10:13], v[2:5], 0
	ds_read2_b64 v[68:71], v32 offset0:5 offset1:207
	v_pk_fma_f16 v2, v52, v6, v2
	v_pk_fma_f16 v3, v53, v7, v3
	v_pk_fma_f16 v4, v54, v8, v4
	v_pk_fma_f16 v5, v55, v9, v5
	v_cndmask_b32_e64 v26, v26, v18, s[60:61]
	s_waitcnt lgkmcnt(8)
	v_pk_fma_f16 v6, v2, v124, v125 op_sel:[0,1,1] op_sel_hi:[1,1,1] neg_lo:[1,0,0] neg_hi:[1,0,0]
	v_pk_fma_f16 v7, v3, v124, v125 op_sel:[0,1,1] op_sel_hi:[1,1,1] neg_lo:[1,0,0] neg_hi:[1,0,0]
	v_pk_fma_f16 v8, v4, v124, v125 op_sel:[0,1,1] op_sel_hi:[1,1,1] neg_lo:[1,0,0] neg_hi:[1,0,0]
	v_pk_fma_f16 v9, v5, v124, v125 op_sel:[0,1,1] op_sel_hi:[1,1,1] neg_lo:[1,0,0] neg_hi:[1,0,0]
	v_mfma_f32_16x16x32_f16 v[18:21], v[10:13], v[2:5], 0
	ds_read2_b64 v[72:75], v32 offset0:6 offset1:208
	ds_read_b128 v[132:135], v33 offset:48
	v_pk_fma_f16 v2, v56, v6, v2
	v_pk_fma_f16 v3, v57, v7, v3
	v_pk_fma_f16 v4, v58, v8, v4
	v_pk_fma_f16 v5, v59, v9, v5
	v_cndmask_b32_e64 v27, v27, v23, s[60:61]
	v_pk_fma_f16 v6, v2, v126, v127 op_sel:[0,1,1] op_sel_hi:[1,1,1] neg_lo:[1,0,0] neg_hi:[1,0,0]
	v_pk_fma_f16 v7, v3, v126, v127 op_sel:[0,1,1] op_sel_hi:[1,1,1] neg_lo:[1,0,0] neg_hi:[1,0,0]
	v_pk_fma_f16 v8, v4, v126, v127 op_sel:[0,1,1] op_sel_hi:[1,1,1] neg_lo:[1,0,0] neg_hi:[1,0,0]
	v_pk_fma_f16 v9, v5, v126, v127 op_sel:[0,1,1] op_sel_hi:[1,1,1] neg_lo:[1,0,0] neg_hi:[1,0,0]
	v_mfma_f32_16x16x32_f16 v[22:25], v[10:13], v[2:5], 0
	ds_read2_b64 v[76:79], v32 offset0:7 offset1:209
	v_pk_fma_f16 v2, v60, v6, v2
	v_pk_fma_f16 v3, v61, v7, v3
	v_pk_fma_f16 v4, v62, v8, v4
	v_pk_fma_f16 v5, v63, v9, v5
	v_cndmask_b32_e64 v28, v28, v20, s[60:61]
	s_waitcnt lgkmcnt(3)
	s_mov_b32 s72, 0
	s_cmp_eq_u32 s70, 0
	s_cbranch_scc1 .Lc1_ndt
	s_cmp_eq_u32 s36, 3
	s_cbranch_scc0 .Lc1_ndt
	s_mov_b32 s72, 1
	ds_read_b32 v45, v36 offset:124
	ds_read_b128 v[112:115], v43 offset:0
	ds_read_b128 v[116:119], v43 offset:1024
